# attention K tile: 16-byte chunks swizzled by (row&15) (conflict-free ds_read_b128 groups) combined with K-fragment reads issued 4 deep ahead of the QK MFMAs (DSA and FoX loops)
# speedup vs baseline: 1.0010x; 1.0010x over previous
; #define LAS __attribute__((address_space(3)))
; __device__ __forceinline__ unsigned xb_xcc_id() { return (unsigned)__builtin_amdgcn_s_getreg((3 << 11) | 20) & 0xFu; }
; __device__ __forceinline__ int v_rd_base(int lane) { return ((lane & 3) << 3) | (((lane >> 2) & 3) << 6) | (((lane >> 4) & 1) << 5) | (((lane >> 5) & 1) << 8); }
; #define PHASE(k) if (IN(k))
; template <int MODE> ...
;     int lane; asm volatile("v_mbcnt_lo_u32_b32 %0, -1, 0\n\tv_mbcnt_hi_u32_b32 %0, -1, %0" : "=v"(lane));
;     const int wid = __builtin_amdgcn_readfirstlane(threadIdx.x >> 6), tid = wid * 64 + lane, r32 = lane & 31, hi = lane >> 5;
;     const int qlo = P0 + wid * QBLK, qm = qlo + r32 - 4 * hi, lastj = qlo / KVBLK;
;     float* wsw = (float*)(lds + OFF_W) + wid * 64; float* li_l = wsw; float* al_l = wsw + 32;
;     const int vb0 = (int)(uintptr_t)lds + v_rd_base(lane);
;     const unsigned ldsb = (unsigned)(uintptr_t)lds;
;     bf16x8 qr[8];
; __global__ void __launch_bounds__(NTHREADS, 2) mega_fwd(Args args) {
;     ...
;     PHASE(5) {
;         LAS unsigned* qsl = (LAS unsigned*)(F.lds + fa::OFF_W + NWAVES * 64 * 4);
;         unsigned* const qctr = (unsigned*)(ws + WS_CTL) + 2048;
;         const int myx = (int)(xb_xcc_id() & 7u);
;         if (MK_ATT_MODES & 1) for (int qi = 0; qi < NH; ++qi) { const int h = (myx + qi) & 7; const size_t ho = (size_t)h * S * HD;
;             for (;;) {
;                 __syncthreads();
;                 { int l0; asm volatile("v_mbcnt_lo_u32_b32 %0, -1, 0\n\tv_mbcnt_hi_u32_b32 %0, -1, %0" : "=v"(l0)); if (wave == 0 && l0 == 0) qsl[0] = __hip_atomic_fetch_add(qctr + 64 * h, 1u, __ATOMIC_RELAXED, __HIP_MEMORY_SCOPE_AGENT); }
;                 __syncthreads();
;                 const unsigned idx = qsl[0]; if (idx >= 48u) break;
;                 const int ent = DSA_TAB[idx], qb = ent & 255, prt = ent >> 8, NTq = 4 * (qb + 1);
;                 const int jb = (prt == 2) ? NTq / 2 : 0, je = (prt == 1) ? NTq / 2 : NTq;
;                 const int slot = (h * 16 + (qb - 16)) * 2 + (prt - 1);
;                 fa::attn_block<0>((char*)lds_raw, PROJ + C_QA + h * HD, args.in[4], ROT, KA + ho, VA + ho, nullptr, nullptr, MASK, nullptr, OB, h * HD, 0, qb * 256, jb, je,
.LBB0_1143:
	v_readlane_b32 s2, v241, 19
	v_readlane_b32 s3, v241, 20
	s_cmp_lt_i32 s2, 6
	s_cselect_b64 s[2:3], -1, 0
	s_and_b64 s[2:3], s[2:3], s[0:1]
	s_andn2_b64 vcc, exec, s[2:3]
	v_mbcnt_lo_u32_b32 v220, -1, 0
	s_cbranch_vccnz .LBB0_1541
	v_writelane_b32 v239, s2, 10
	v_readlane_b32 s0, v241, 5
	v_readlane_b32 s1, v241, 6
	v_writelane_b32 v239, s3, 11
	s_add_u32 s13, s0, 0x2000
	s_getreg_b32 s2, hwreg(HW_REG_XCC_ID, 0, 4)
	s_addc_u32 s28, s1, 0
	v_writelane_b32 v239, s2, 58
	v_readlane_b32 s2, v241, 0
	s_cmp_lt_u32 s2, 64
	s_cselect_b64 s[2:3], -1, 0
	s_add_u32 s29, s0, 0x41500000
	s_addc_u32 s30, s1, 0
	s_add_u32 s8, s0, 0x700000
	s_addc_u32 s9, s1, 0
	s_add_u32 s31, s0, 0x4b500000
	s_addc_u32 s34, s1, 0
	s_add_u32 s35, s0, 0x4c500000
	s_addc_u32 s36, s1, 0
	s_add_u32 s37, s0, 0x52700000
	s_addc_u32 s38, s1, 0
	s_add_u32 s39, s0, 0x52f00000
	s_addc_u32 s40, s1, 0
	s_add_u32 s41, s0, 0x63000000
	s_addc_u32 s42, s1, 0
	s_add_u32 s43, s0, 0x65000000
	s_addc_u32 s44, s1, 0
	s_add_u32 s45, s0, 0x52700010
	s_addc_u32 s46, s1, 0
	s_add_u32 s47, s0, 0x52700008
	s_addc_u32 s48, s1, 0
	s_add_i32 s49, 0, 0x11800
	v_writelane_b32 v240, s2, 6
	s_mov_b32 s11, 0
	v_mov_b32_e32 v179, 0
	v_mov_b32_e32 v186, 0x358637bd
	v_mov_b32_e32 v187, 0x260
	s_movk_i32 s50, 0xf0
	s_movk_i32 s51, 0xff00
	s_mov_b32 s52, 0xff800000
	s_mov_b32 s53, 0x41000000
	s_mov_b32 s12, 0x3e0293ee
	v_mov_b32_e32 v188, s49
	v_mov_b32_e32 v189, 0xf149f2ca
	v_mbcnt_hi_u32_b32 v1, -1, v220
	s_mov_b32 s54, 0
	v_writelane_b32 v240, s3, 7
	s_branch .LBB0_1146

; __device__ __forceinline__ float bf_lo(unsigned w) { return __uint_as_float(w << 16); }
; template <int MODE> ...
;     int lane; asm volatile("v_mbcnt_lo_u32_b32 %0, -1, 0\n\tv_mbcnt_hi_u32_b32 %0, -1, %0" : "=v"(lane));
;     const int wid = __builtin_amdgcn_readfirstlane(threadIdx.x >> 6), tid = wid * 64 + lane, r32 = lane & 31, hi = lane >> 5;
;     const int qlo = P0 + wid * QBLK, qm = qlo + r32 - 4 * hi, lastj = qlo / KVBLK;
;     float* wsw = (float*)(lds + OFF_W) + wid * 64; float* li_l = wsw; float* al_l = wsw + 32;
;     const int vb0 = (int)(uintptr_t)lds + v_rd_base(lane);
;     const unsigned ldsb = (unsigned)(uintptr_t)lds;
;     bf16x8 qr[8];
;     { const bf16_t* qrow = Qh + (size_t)(qlo + r32) * NINP + hi * 8; float qv[8][8]; float ss = 0.f;
; #pragma unroll
;       for (int d0 = 0; d0 < 8; ++d0) { const u32x4 w = *reinterpret_cast<const u32x4*>(qrow + d0 * 16);
;           qv[d0][0] = bf_lo(w.x); qv[d0][1] = bf_hi(w.x); qv[d0][2] = bf_lo(w.y); qv[d0][3] = bf_hi(w.y); qv[d0][4] = bf_lo(w.z); qv[d0][5] = bf_hi(w.z); qv[d0][6] = bf_lo(w.w); qv[d0][7] = bf_hi(w.w);
; #pragma unroll
;           for (int j = 0; j < 8; ++j) ss = fmaf(qv[d0][j], qv[d0][j], ss); }
;       { auto rr = __builtin_amdgcn_permlane32_swap(__float_as_uint(ss), __float_as_uint(ss), false, false); ss = __uint_as_float(rr[0]) + __uint_as_float(rr[1]); }
;       const float rstd = 1.f / sqrtf(ss * (1.f / HD) + RMS_EPS);
; __global__ void __launch_bounds__(NTHREADS, 2) mega_fwd(Args args) {
;     ...
;                 __syncthreads();
;                 { int l0; asm volatile("v_mbcnt_lo_u32_b32 %0, -1, 0\n\tv_mbcnt_hi_u32_b32 %0, -1, %0" : "=v"(l0)); if (wave == 0 && l0 == 0) qsl[0] = __hip_atomic_fetch_add(qctr + 64 * h, 1u, __ATOMIC_RELAXED, __HIP_MEMORY_SCOPE_AGENT); }
;                 __syncthreads();
;                 const unsigned idx = qsl[0]; if (idx >= 48u) break;
;                 const int ent = DSA_TAB[idx], qb = ent & 255, prt = ent >> 8, NTq = 4 * (qb + 1);
;                 const int jb = (prt == 2) ? NTq / 2 : 0, je = (prt == 1) ? NTq / 2 : NTq;
;                 const int slot = (h * 16 + (qb - 16)) * 2 + (prt - 1);
;                 fa::attn_block<0>((char*)lds_raw, PROJ + C_QA + h * HD, args.in[4], ROT, KA + ho, VA + ho, nullptr, nullptr, MASK, nullptr, OB, h * HD, 0, qb * 256, jb, je,
.LBB0_1154:
	s_or_b64 exec, exec, s[0:1]
	s_waitcnt lgkmcnt(0)
	s_barrier
	ds_read_b32 v2, v188
	s_mov_b64 s[0:1], -1
	s_waitcnt lgkmcnt(0)
	v_cmp_lt_u32_e32 vcc, 47, v2
	v_readfirstlane_b32 s10, v2
	s_cbranch_vccnz .LBB0_1149
	s_lshl_b64 s[0:1], s[10:11], 1
	s_getpc_b64 s[2:3]
	s_add_u32 s2, s2, _ZL7DSA_TAB@rel32@lo+4
	s_addc_u32 s3, s3, _ZL7DSA_TAB@rel32@hi+12
	s_add_u32 s0, s2, s0
	s_addc_u32 s1, s3, s1
	global_load_ushort v12, v179, s[0:1]
	v_mbcnt_lo_u32_b32 v192, -1, 0
	v_mbcnt_hi_u32_b32 v192, -1, v192
	v_readfirstlane_b32 s4, v0
	v_ashrrev_i32_e32 v191, 5, v192
	v_lshlrev_b32_e32 v58, 3, v191
	v_ashrrev_i32_e32 v59, 31, v58
	v_lshl_add_u64 v[14:15], v[58:59], 2, s[84:85]
	global_load_dwordx4 v[6:9], v[14:15], off
	global_load_dwordx4 v[2:5], v[14:15], off offset:16
	global_load_dwordx4 v[70:73], v[14:15], off offset:64
	global_load_dwordx4 v[64:67], v[14:15], off offset:80
	v_and_b32_e32 v190, 31, v192
	v_mov_b64_e32 v[10:11], s[16:17]
	v_lshlrev_b32_e32 v207, 4, v191
	v_lshlrev_b32_e32 v199, 4, v190
	v_mov_b32_e32 v195, 1.0
	v_lshlrev_b32_e32 v198, 8, v190
	v_lshlrev_b32_e32 v193, 2, v191
	v_bitop3_b32 v202, v199, v207, s50 bitop3:0x6c
	v_add_u32_e32 v203, 32, v207
	v_add_u32_e32 v201, 64, v207
	v_add_u32_e32 v200, 0x60, v207
	s_waitcnt vmcnt(4)
	v_readfirstlane_b32 s0, v12
	s_and_b32 s57, s0, 0xff
	s_lshl_b32 s71, s57, 2
	s_add_i32 s2, s71, 4
	s_lshr_b32 s58, s0, 8
	s_lshr_b32 s3, s2, 1
	s_cmp_eq_u32 s58, 2
	s_cselect_b32 s61, s3, 0
	s_lshr_b32 s5, s4, 6
	s_lshl_b32 s0, s57, 8
	s_lshl_b32 s56, s5, 5
	s_add_i32 s59, s56, s0
	v_or_b32_e32 v178, s59, v190
	s_movk_i32 s0, 0x4200
	v_mad_u64_u32 v[10:11], s[0:1], v178, s0, v[10:11]
	v_lshl_add_u64 v[10:11], v[58:59], 1, v[10:11]
	global_load_dwordx4 v[74:77], v[10:11], off offset:64
	global_load_dwordx4 v[78:81], v[10:11], off offset:96
	global_load_dwordx4 v[82:85], v[10:11], off offset:128
	global_load_dwordx4 v[88:91], v[10:11], off offset:160
	global_load_dwordx4 v[92:95], v[10:11], off offset:192
	global_load_dwordx4 v[136:139], v[10:11], off offset:224
	global_load_dwordx4 v[140:143], v[10:11], off
	global_load_dwordx4 v[144:147], v[10:11], off offset:32
	global_load_dwordx4 v[50:53], v[14:15], off offset:144
	global_load_dwordx4 v[54:57], v[14:15], off offset:128
	global_load_dwordx4 v[42:45], v[14:15], off offset:208
	global_load_dwordx4 v[46:49], v[14:15], off offset:192
	global_load_dwordx4 v[34:37], v[14:15], off offset:272
	global_load_dwordx4 v[38:41], v[14:15], off offset:256
	global_load_dwordx4 v[26:29], v[14:15], off offset:336
	global_load_dwordx4 v[30:33], v[14:15], off offset:320
	global_load_dwordx4 v[18:21], v[14:15], off offset:400
	global_load_dwordx4 v[22:25], v[14:15], off offset:384
	global_load_dwordx4 v[10:13], v[14:15], off offset:464
	s_nop 0
	global_load_dwordx4 v[14:17], v[14:15], off offset:448
	s_waitcnt vmcnt(22)
	v_mov_b32_e32 v63, v4
	s_waitcnt vmcnt(20)
	v_mov_b32_e32 v4, v67
	v_mov_b32_e32 v67, v2
	v_mov_b32_e32 v2, v65
	v_mov_b32_e32 v65, v8
	v_mov_b32_e32 v8, v73
	v_mov_b32_e32 v69, v6
	v_mov_b32_e32 v6, v71
	v_mov_b32_e32 v62, v66
	v_mov_b32_e32 v66, v64
	v_mov_b32_e32 v64, v72
	v_mov_b32_e32 v68, v70
	s_mov_b32 s0, 0xf800000
	v_lshlrev_b64 v[60:61], 7, v[178:179]
	v_lshl_add_u64 v[60:61], s[8:9], 0, v[60:61]
	s_andn2_b32 s4, s4, 63
	s_lshr_b32 s60, s59, 6
	s_lshl_b32 s73, s61, 14
	s_add_u32 s6, s18, s73
	v_add_u32_e32 v86, s4, v192
	s_addc_u32 s7, s19, 0
	s_lshl_b32 s72, s5, 10
	s_cmp_lg_u32 0, -1
	v_lshlrev_b32_e32 v178, 10, v178
	s_waitcnt vmcnt(19)
	v_lshlrev_b32_e32 v132, 16, v77
	s_waitcnt vmcnt(18)
	v_lshlrev_b32_e32 v122, 16, v81
	s_waitcnt vmcnt(17)
	v_lshlrev_b32_e32 v114, 16, v85
	v_and_b32_e32 v111, 0xffff0000, v85
	v_lshlrev_b32_e32 v112, 16, v83
	v_and_b32_e32 v108, 0xffff0000, v83
	s_waitcnt vmcnt(13)
	v_lshlrev_b32_e32 v85, 16, v140
	v_and_b32_e32 v83, 0xffff0000, v140
	v_fma_f32 v135, v85, v85, 0
	v_and_b32_e32 v119, 0xffff0000, v81
	v_lshlrev_b32_e32 v81, 16, v141
	v_fmac_f32_e32 v135, v83, v83
	v_lshlrev_b32_e32 v120, 16, v79
	v_and_b32_e32 v116, 0xffff0000, v79
	v_and_b32_e32 v79, 0xffff0000, v141
	v_fmac_f32_e32 v135, v81, v81
	v_and_b32_e32 v130, 0xffff0000, v77
	v_lshlrev_b32_e32 v77, 16, v142
	v_fmac_f32_e32 v135, v79, v79
	v_lshlrev_b32_e32 v127, 16, v75
	v_and_b32_e32 v126, 0xffff0000, v75
	v_and_b32_e32 v75, 0xffff0000, v142
	v_fmac_f32_e32 v135, v77, v77
	v_lshlrev_b32_e32 v73, 16, v143
	v_fmac_f32_e32 v135, v75, v75
	v_and_b32_e32 v71, 0xffff0000, v143
	v_fmac_f32_e32 v135, v73, v73
	v_lshlrev_b32_e32 v121, 16, v84
	v_and_b32_e32 v117, 0xffff0000, v84
	s_waitcnt vmcnt(12)
; __device__ __forceinline__ float bf_lo(unsigned w) { return __uint_as_float(w << 16); }
; __device__ __forceinline__ float bf_hi(unsigned w) { return __uint_as_float(w & 0xffff0000u); }
; template <int MODE> ...
;     ...
;     { const bf16_t* qrow = Qh + (size_t)(qlo + r32) * NINP + hi * 8; float qv[8][8]; float ss = 0.f;
; #pragma unroll
;       for (int d0 = 0; d0 < 8; ++d0) { const u32x4 w = *reinterpret_cast<const u32x4*>(qrow + d0 * 16);
;           qv[d0][0] = bf_lo(w.x); qv[d0][1] = bf_hi(w.x); qv[d0][2] = bf_lo(w.y); qv[d0][3] = bf_hi(w.y); qv[d0][4] = bf_lo(w.z); qv[d0][5] = bf_hi(w.z); qv[d0][6] = bf_lo(w.w); qv[d0][7] = bf_hi(w.w);
; #pragma unroll
;           for (int j = 0; j < 8; ++j) ss = fmaf(qv[d0][j], qv[d0][j], ss); }
;       { auto rr = __builtin_amdgcn_permlane32_swap(__float_as_uint(ss), __float_as_uint(ss), false, false); ss = __uint_as_float(rr[0]) + __uint_as_float(rr[1]); }
;       const float rstd = 1.f / sqrtf(ss * (1.f / HD) + RMS_EPS);
; #pragma unroll
;       for (int d0 = 0; d0 < 8; ++d0) { const f32x4 g0 = *(const f32x4*)(qgain + d0 * 16 + hi * 8), g1 = *(const f32x4*)(qgain + d0 * 16 + hi * 8 + 4);
; #pragma unroll
;           for (int j = 0; j < 4; ++j) { qv[d0][j] *= rstd * g0[j]; qv[d0][4 + j] *= rstd * g1[j]; } }
;       if (MODE == 0) { const float* rp = rot + ((size_t)(qlo + r32) * 16 + hi * 8) * 2;
	v_lshlrev_b32_e32 v84, 16, v144
	v_fmac_f32_e32 v135, v71, v71
	v_lshlrev_b32_e32 v118, 16, v82
	v_and_b32_e32 v115, 0xffff0000, v82
	v_and_b32_e32 v82, 0xffff0000, v144
	v_fmac_f32_e32 v135, v84, v84
	v_lshlrev_b32_e32 v125, 16, v80
	v_and_b32_e32 v124, 0xffff0000, v80
	v_lshlrev_b32_e32 v80, 16, v145
	v_fmac_f32_e32 v135, v82, v82
	v_lshlrev_b32_e32 v131, 16, v78
	v_and_b32_e32 v123, 0xffff0000, v78
	v_and_b32_e32 v78, 0xffff0000, v145
	v_fmac_f32_e32 v135, v80, v80
	v_lshlrev_b32_e32 v134, 16, v76
	v_and_b32_e32 v133, 0xffff0000, v76
	v_lshlrev_b32_e32 v76, 16, v146
	v_fmac_f32_e32 v135, v78, v78
	v_lshlrev_b32_e32 v129, 16, v74
	v_and_b32_e32 v128, 0xffff0000, v74
	v_and_b32_e32 v74, 0xffff0000, v146
	v_fmac_f32_e32 v135, v76, v76
	v_lshlrev_b32_e32 v72, 16, v147
	v_fmac_f32_e32 v135, v74, v74
	v_and_b32_e32 v70, 0xffff0000, v147
	v_fmac_f32_e32 v135, v72, v72
	v_fmac_f32_e32 v135, v70, v70
	v_fmac_f32_e32 v135, v129, v129
	v_fmac_f32_e32 v135, v128, v128
	v_fmac_f32_e32 v135, v127, v127
	v_fmac_f32_e32 v135, v126, v126
	v_fmac_f32_e32 v135, v134, v134
	v_fmac_f32_e32 v135, v133, v133
	v_fmac_f32_e32 v135, v132, v132
	v_fmac_f32_e32 v135, v130, v130
	v_fmac_f32_e32 v135, v131, v131
	v_fmac_f32_e32 v135, v123, v123
	v_fmac_f32_e32 v135, v120, v120
	v_fmac_f32_e32 v135, v116, v116
	v_fmac_f32_e32 v135, v125, v125
	v_fmac_f32_e32 v135, v124, v124
	v_fmac_f32_e32 v135, v122, v122
	v_fmac_f32_e32 v135, v119, v119
	v_fmac_f32_e32 v135, v118, v118
	v_fmac_f32_e32 v135, v115, v115
	v_fmac_f32_e32 v135, v112, v112
	v_fmac_f32_e32 v135, v108, v108
	v_fmac_f32_e32 v135, v121, v121
	v_fmac_f32_e32 v135, v117, v117
	v_fmac_f32_e32 v135, v114, v114
	v_lshlrev_b32_e32 v110, 16, v88
	v_fmac_f32_e32 v135, v111, v111
	v_and_b32_e32 v107, 0xffff0000, v88
	v_fmac_f32_e32 v135, v110, v110
	v_lshlrev_b32_e32 v104, 16, v89
	v_fmac_f32_e32 v135, v107, v107
	v_and_b32_e32 v100, 0xffff0000, v89
	v_fmac_f32_e32 v135, v104, v104
	v_lshlrev_b32_e32 v113, 16, v90
	v_fmac_f32_e32 v135, v100, v100
	v_and_b32_e32 v109, 0xffff0000, v90
	v_fmac_f32_e32 v135, v113, v113
	v_lshlrev_b32_e32 v106, 16, v91
	v_fmac_f32_e32 v135, v109, v109
	v_and_b32_e32 v103, 0xffff0000, v91
	v_fmac_f32_e32 v135, v106, v106
	v_lshlrev_b32_e32 v102, 16, v92
	v_fmac_f32_e32 v135, v103, v103
	v_and_b32_e32 v99, 0xffff0000, v92
	v_fmac_f32_e32 v135, v102, v102
	v_lshlrev_b32_e32 v96, 16, v93
	v_fmac_f32_e32 v135, v99, v99
	v_and_b32_e32 v92, 0xffff0000, v93
	v_fmac_f32_e32 v135, v96, v96
	v_lshlrev_b32_e32 v105, 16, v94
	v_fmac_f32_e32 v135, v92, v92
	v_and_b32_e32 v101, 0xffff0000, v94
	v_fmac_f32_e32 v135, v105, v105
	v_lshlrev_b32_e32 v98, 16, v95
	v_fmac_f32_e32 v135, v101, v101
	v_and_b32_e32 v95, 0xffff0000, v95
	v_fmac_f32_e32 v135, v98, v98
	v_lshlrev_b32_e32 v94, 16, v136
	v_fmac_f32_e32 v135, v95, v95
	v_and_b32_e32 v91, 0xffff0000, v136
	v_fmac_f32_e32 v135, v94, v94
	v_lshlrev_b32_e32 v89, 16, v137
	v_fmac_f32_e32 v135, v91, v91
	v_and_b32_e32 v87, 0xffff0000, v137
	v_fmac_f32_e32 v135, v89, v89
	v_lshlrev_b32_e32 v97, 16, v138
	v_fmac_f32_e32 v135, v87, v87
	v_and_b32_e32 v93, 0xffff0000, v138
	v_fmac_f32_e32 v135, v97, v97
	v_lshlrev_b32_e32 v90, 16, v139
	v_fmac_f32_e32 v135, v93, v93
	v_and_b32_e32 v88, 0xffff0000, v139
	v_fmac_f32_e32 v135, v90, v90
	v_fmac_f32_e32 v135, v88, v88
	v_mov_b32_e32 v136, v135
	s_nop 1
	v_permlane32_swap_b32_e32 v135, v136
	v_add_f32_e32 v135, v135, v136
	v_fmamk_f32 v135, v135, 0x3c000000, v186
	v_mul_f32_e32 v136, 0x4f800000, v135
	v_cmp_gt_f32_e32 vcc, s0, v135
	v_lshl_add_u64 v[144:145], v[58:59], 3, v[60:61]
	s_nop 0
	v_cndmask_b32_e32 v135, v135, v136, vcc
	v_sqrt_f32_e32 v140, v135
	global_load_dwordx4 v[58:61], v[144:145], off offset:48
	global_load_dwordx4 v[136:139], v[144:145], off offset:32
	v_add_u32_e32 v141, -1, v140
	v_add_u32_e32 v142, 1, v140
	v_fma_f32 v143, -v141, v140, v135
	v_fma_f32 v146, -v142, v140, v135
	v_cmp_ge_f32_e64 s[0:1], 0, v143
	s_nop 1
	v_cndmask_b32_e64 v140, v140, v141, s[0:1]
	v_cmp_lt_f32_e64 s[0:1], 0, v146
	s_nop 1
	v_cndmask_b32_e64 v140, v140, v142, s[0:1]
	v_mul_f32_e32 v141, 0x37800000, v140
	v_cndmask_b32_e32 v140, v140, v141, vcc
	v_cmp_class_f32_e32 vcc, v135, v187
	s_nop 1
	v_cndmask_b32_e32 v135, v140, v135, vcc
	global_load_dwordx4 v[140:143], v[144:145], off offset:16
	s_nop 0
	global_load_dwordx4 v[144:147], v[144:145], off
	v_div_scale_f32 v148, s[0:1], v135, v135, 1.0
	v_rcp_f32_e32 v149, v148
	v_div_scale_f32 v150, vcc, 1.0, v135, 1.0
	s_movk_i32 s0, 0xf0
	v_fma_f32 v151, -v148, v149, 1.0
	v_fmac_f32_e32 v149, v151, v149
	v_mul_f32_e32 v151, v150, v149
	v_fma_f32 v152, -v148, v151, v150
	v_fmac_f32_e32 v151, v152, v149
	v_fma_f32 v148, -v148, v151, v150
	v_div_fmas_f32 v148, v148, v149, v151
	v_div_fixup_f32 v148, v148, v135, 1.0
	v_pk_mul_f32 v[4:5], v[4:5], v[148:149] op_sel_hi:[1,0]
	s_waitcnt vmcnt(5)
	v_mul_f32_e32 v10, v148, v10
	v_pk_mul_f32 v[4:5], v[4:5], v[70:71]
	v_mul_f32_e32 v70, v10, v97
	s_waitcnt vmcnt(4)
; __device__ __forceinline__ unsigned cvt_pk_bf16(float lo, float hi) { unsigned r; asm volatile("v_cvt_pk_bf16_f32 %0, %1, %2" : "=v"(r) : "v"(lo), "v"(hi)); return r; }
; template <int MODE> ...
;     ...
;       for (int d0 = 0; d0 < 8; ++d0) { const f32x4 g0 = *(const f32x4*)(qgain + d0 * 16 + hi * 8), g1 = *(const f32x4*)(qgain + d0 * 16 + hi * 8 + 4);
; #pragma unroll
;           for (int j = 0; j < 4; ++j) { qv[d0][j] *= rstd * g0[j]; qv[d0][4 + j] *= rstd * g1[j]; } }
;       if (MODE == 0) { const float* rp = rot + ((size_t)(qlo + r32) * 16 + hi * 8) * 2;
; #pragma unroll
;           for (int j = 0; j < 8; j += 2) { const f32x4 cs = *(const f32x4*)(rp + 2 * j);
;               { const float x1 = qv[0][j], x2 = qv[1][j]; qv[0][j] = x1 * cs[0] - x2 * cs[1]; qv[1][j] = x2 * cs[0] + x1 * cs[1]; }
;               { const float x1 = qv[0][j + 1], x2 = qv[1][j + 1]; qv[0][j + 1] = x1 * cs[2] - x2 * cs[3]; qv[1][j + 1] = x2 * cs[2] + x1 * cs[3]; } } }
; #pragma unroll
;       for (int d0 = 0; d0 < 8; ++d0) { u32x4 w; w.x = cvt_pk_bf16(qv[d0][0], qv[d0][1]); w.y = cvt_pk_bf16(qv[d0][2], qv[d0][3]); w.z = cvt_pk_bf16(qv[d0][4], qv[d0][5]); w.w = cvt_pk_bf16(qv[d0][6], qv[d0][7]);
;           qr[d0] = *reinterpret_cast<bf16x8*>(&w); } }
;     bf16x8 qx = (bf16x8){0, 0, 0, 0, 0, 0, 0, 0};
;     if (MODE == 1 && hi == 0) qx = *reinterpret_cast<const bf16x8*>(QXh + (size_t)(qlo + r32) * 8);
;     unsigned koff[2], voff[2];
; #pragma unroll
;     for (int i = 0; i < 2; ++i) { const int q = tid * 16 + i * 8192;
;         { const int row = q >> 8, colB = (q & 255) ^ ((row & 7) << 4); koff[i] = (unsigned)(row * 256 + colB); }
;         { const int sb = q >> 9, w = q & 511, kk = (sb >> 2) * 8 + (w >> 6), k = (kk & ~0xC) | ((kk & 4) << 1) | ((kk & 8) >> 1), col = (sb & 3) * 32 + ((w & 63) >> 4) * 8; voff[i] = (unsigned)(k * 256 + col * 2); } }
	v_mul_f32_e32 v10, v148, v15
	v_mul_f32_e32 v15, v10, v91
	v_mul_f32_e32 v10, v148, v11
	v_mul_f32_e32 v71, v10, v93
	v_mul_f32_e32 v10, v148, v16
	v_mul_f32_e32 v16, v10, v89
	v_mul_f32_e32 v10, v148, v12
	v_pk_mul_f32 v[68:69], v[68:69], v[148:149] op_sel_hi:[1,0]
	v_mul_f32_e32 v12, v10, v90
	v_mul_f32_e32 v10, v148, v17
	v_pk_mul_f32 v[66:67], v[66:67], v[148:149] op_sel_hi:[1,0]
	v_pk_mul_f32 v[6:7], v[6:7], v[148:149] op_sel_hi:[1,0]
	v_pk_mul_f32 v[2:3], v[2:3], v[148:149] op_sel_hi:[1,0]
	v_pk_mul_f32 v[64:65], v[64:65], v[148:149] op_sel_hi:[1,0]
	v_pk_mul_f32 v[62:63], v[62:63], v[148:149] op_sel_hi:[1,0]
	v_pk_mul_f32 v[8:9], v[8:9], v[148:149] op_sel_hi:[1,0]
	v_mul_f32_e32 v149, v148, v50
	v_mul_f32_e32 v151, v148, v51
	v_pk_mul_f32 v[50:51], v[68:69], v[84:85]
	v_mul_f32_e32 v17, v10, v87
	v_mul_f32_e32 v10, v148, v13
	v_mul_f32_e32 v13, v10, v88
	v_mul_f32_e32 v152, v56, v148
	v_mul_f32_e32 v154, v57, v148
	v_pk_mul_f32 v[6:7], v[6:7], v[82:83]
	v_pk_mul_f32 v[56:57], v[62:63], v[72:73]
	v_mul_f32_e32 v135, v54, v148
	v_mul_f32_e32 v150, v55, v148
	v_pk_mul_f32 v[54:55], v[64:65], v[80:81]
	v_pk_mul_f32 v[8:9], v[8:9], v[78:79]
	v_mul_f32_e32 v153, v148, v52
	v_mul_f32_e32 v155, v148, v53
	v_pk_mul_f32 v[52:53], v[66:67], v[76:77]
	v_pk_mul_f32 v[2:3], v[2:3], v[74:75]
	v_mul_f32_e32 v46, v148, v46
	v_mul_f32_e32 v63, v149, v134
	v_mul_f32_e32 v64, v150, v128
	v_mul_f32_e32 v65, v151, v133
	v_mul_f32_e32 v66, v152, v127
	v_mul_f32_e32 v67, v153, v132
	v_mul_f32_e32 v42, v148, v42
	v_mul_f32_e32 v47, v148, v47
	v_mul_f32_e32 v43, v148, v43
	v_mul_f32_e32 v48, v148, v48
	v_mul_f32_e32 v44, v148, v44
	v_mul_f32_e32 v49, v148, v49
	v_mul_f32_e32 v45, v148, v45
	v_mul_f32_e32 v38, v148, v38
	v_mul_f32_e32 v34, v148, v34
	v_mul_f32_e32 v39, v148, v39
	v_mul_f32_e32 v35, v148, v35
	v_mul_f32_e32 v40, v148, v40
	v_mul_f32_e32 v36, v148, v36
	v_mul_f32_e32 v41, v148, v41
	v_mul_f32_e32 v37, v148, v37
	v_mul_f32_e32 v30, v148, v30
	v_mul_f32_e32 v26, v148, v26
	v_mul_f32_e32 v31, v148, v31
	v_mul_f32_e32 v27, v148, v27
	v_mul_f32_e32 v32, v148, v32
	v_mul_f32_e32 v28, v148, v28
	s_waitcnt vmcnt(0)
	v_pk_mul_f32 v[10:11], v[50:51], v[144:145] op_sel:[1,0] op_sel_hi:[0,1]
	v_sub_f32_e32 v72, v10, v11
	v_pk_mul_f32 v[10:11], v[50:51], v[144:145]
	v_mul_f32_e32 v33, v148, v33
	v_add_f32_e32 v50, v11, v10
	v_pk_mul_f32 v[10:11], v[6:7], v[146:147] op_sel:[1,0] op_sel_hi:[0,1]
	v_pk_mul_f32 v[6:7], v[6:7], v[146:147]
	v_sub_f32_e32 v10, v10, v11
	v_add_f32_e32 v11, v7, v6
	v_pk_mul_f32 v[6:7], v[54:55], v[140:141] op_sel:[1,0] op_sel_hi:[0,1]
	v_sub_f32_e32 v51, v6, v7
	v_pk_mul_f32 v[6:7], v[54:55], v[140:141]
	v_mul_f32_e32 v29, v148, v29
	v_add_f32_e32 v54, v7, v6
	v_pk_mul_f32 v[6:7], v[8:9], v[142:143] op_sel:[1,0] op_sel_hi:[0,1]
	v_sub_f32_e32 v55, v6, v7
	v_pk_mul_f32 v[6:7], v[8:9], v[142:143]
	v_mul_f32_e32 v22, v148, v22
	v_add_f32_e32 v8, v7, v6
	v_pk_mul_f32 v[6:7], v[52:53], v[136:137] op_sel:[1,0] op_sel_hi:[0,1]
	v_sub_f32_e32 v9, v6, v7
	v_pk_mul_f32 v[6:7], v[52:53], v[136:137]
	v_mul_f32_e32 v18, v148, v18
	v_add_f32_e32 v52, v7, v6
	v_pk_mul_f32 v[6:7], v[2:3], v[138:139] op_sel:[1,0] op_sel_hi:[0,1]
	v_pk_mul_f32 v[2:3], v[2:3], v[138:139]
	v_sub_f32_e32 v6, v6, v7
	v_add_f32_e32 v7, v3, v2
	v_pk_mul_f32 v[2:3], v[56:57], v[58:59] op_sel:[1,0] op_sel_hi:[0,1]
	v_sub_f32_e32 v53, v2, v3
	v_pk_mul_f32 v[2:3], v[56:57], v[58:59]
	v_mul_f32_e32 v23, v148, v23
	v_add_f32_e32 v56, v3, v2
	v_pk_mul_f32 v[2:3], v[4:5], v[60:61] op_sel:[1,0] op_sel_hi:[0,1]
	v_sub_f32_e32 v57, v2, v3
	v_pk_mul_f32 v[2:3], v[4:5], v[60:61]
	v_mul_f32_e32 v19, v148, v19
	v_add_f32_e32 v2, v3, v2
	v_mul_f32_e32 v24, v148, v24
	v_mul_f32_e32 v20, v148, v20
	v_mul_f32_e32 v25, v148, v25
	v_mul_f32_e32 v21, v148, v21
	v_mul_f32_e32 v14, v148, v14
	v_cvt_pk_bf16_f32 v146, v72, v10
	v_cvt_pk_bf16_f32 v147, v51, v55
	v_cvt_pk_bf16_f32 v148, v9, v6
	v_cvt_pk_bf16_f32 v149, v53, v57
	v_cvt_pk_bf16_f32 v150, v50, v11
	v_cvt_pk_bf16_f32 v151, v54, v8
	v_cvt_pk_bf16_f32 v152, v52, v7
	v_cvt_pk_bf16_f32 v153, v56, v2
	v_lshlrev_b32_e32 v2, 4, v86
	v_and_b32_e32 v3, 0xf0, v86
	v_bitop3_b32 v3, v2, v3, s0 bitop3:0x6c
	s_cselect_b32 s0, 0, 0
	s_add_i32 s63, s72, s0
	v_mul_f32_e32 v62, v135, v129
	v_mul_f32_e32 v68, v154, v126
	v_mul_f32_e32 v69, v155, v130
	v_mul_f32_e32 v46, v46, v131
	v_mul_f32_e32 v42, v42, v125
	v_mul_f32_e32 v47, v47, v123
	v_mul_f32_e32 v43, v43, v124
	v_mul_f32_e32 v48, v48, v120
	v_mul_f32_e32 v44, v44, v122
	v_mul_f32_e32 v49, v49, v116
	v_mul_f32_e32 v45, v45, v119
	v_mul_f32_e32 v38, v38, v118
	v_mul_f32_e32 v34, v34, v121
	v_mul_f32_e32 v39, v39, v115
	v_mul_f32_e32 v35, v35, v117
	v_mul_f32_e32 v40, v40, v112
	v_mul_f32_e32 v36, v36, v114
	v_mul_f32_e32 v41, v41, v108
	v_mul_f32_e32 v37, v37, v111
	v_mul_f32_e32 v30, v30, v110
	v_mul_f32_e32 v26, v26, v113
	v_mul_f32_e32 v31, v31, v107
	v_mul_f32_e32 v27, v27, v109
	v_mul_f32_e32 v32, v32, v104
	v_mul_f32_e32 v28, v28, v106
	v_mul_f32_e32 v33, v33, v100
	v_mul_f32_e32 v29, v29, v103
	v_mul_f32_e32 v22, v22, v102
	v_mul_f32_e32 v18, v18, v105
	v_mul_f32_e32 v23, v23, v99
	v_mul_f32_e32 v19, v19, v101
	v_mul_f32_e32 v24, v24, v96
	v_mul_f32_e32 v20, v20, v98
	v_mul_f32_e32 v25, v25, v92
	v_mul_f32_e32 v21, v21, v95
	v_mul_f32_e32 v14, v14, v94
	v_cvt_pk_bf16_f32 v154, v62, v64
	v_cvt_pk_bf16_f32 v155, v66, v68
	v_cvt_pk_bf16_f32 v156, v63, v65
	v_cvt_pk_bf16_f32 v157, v67, v69
	v_cvt_pk_bf16_f32 v158, v46, v47
	v_cvt_pk_bf16_f32 v159, v48, v49
	v_cvt_pk_bf16_f32 v160, v42, v43
	v_cvt_pk_bf16_f32 v161, v44, v45
	v_cvt_pk_bf16_f32 v142, v38, v39
	v_cvt_pk_bf16_f32 v143, v40, v41
	v_cvt_pk_bf16_f32 v144, v34, v35
	v_cvt_pk_bf16_f32 v145, v36, v37
	v_cvt_pk_bf16_f32 v138, v30, v31
	v_cvt_pk_bf16_f32 v139, v32, v33
	v_cvt_pk_bf16_f32 v140, v26, v27
	v_cvt_pk_bf16_f32 v141, v28, v29
	v_cvt_pk_bf16_f32 v134, v22, v23
	v_cvt_pk_bf16_f32 v135, v24, v25
	v_cvt_pk_bf16_f32 v136, v18, v19
	v_cvt_pk_bf16_f32 v137, v20, v21
	v_cvt_pk_bf16_f32 v130, v14, v15
	v_cvt_pk_bf16_f32 v131, v16, v17
	v_cvt_pk_bf16_f32 v132, v70, v71
	v_cvt_pk_bf16_f32 v133, v12, v13
	v_and_or_b32 v204, v2, s51, v3
	v_add_u32_e32 v2, 0x2000, v2
	s_barrier
; #define VM_WAIT() asm volatile("s_waitcnt vmcnt(0)" ::: "memory")
; #define KDMA(k0, bf) do { const bf16_t* kb_ = Kh + (size_t)(k0) * D; _Pragma("unroll") for (int i_ = 0; i_ < 2; ++i_) pg8::glds16_s((const void*)kb_, koff[i_], ldsb + OFF_K + (bf) * SHM_K + wid * 1024 + i_ * 8192); } while (0)
; #define VDMA(k0, bf) do { const bf16_t* vb_ = Vh + (size_t)(k0) * D; _Pragma("unroll") for (int i_ = 0; i_ < 2; ++i_) pg8::glds16_s((const void*)vb_, voff[i_], ldsb + OFF_V + (bf) * SHM_V + wid * 1024 + i_ * 8192); } while (0)
; template <int KB, bool EXT>
; __device__ __forceinline__ void qkt(f32x16& p0, f32x16& p1, const char* lds, int r32, int hi, const bf16x8* qr, bf16x8 qx) {
;     ...
;     for (int dd = 0; dd < 4; ++dd) kb[dd] = lds + OFF_K + KB * SHM_K + KSWZ(r32, (dd * 16 + hi * 8) * 2);
; #pragma unroll
;     for (int d0 = 0; d0 < 8; ++d0) { const char* a = kb[d0 & 3] + (d0 >> 2) * 128;
;         bf16x8 b0 = *reinterpret_cast<const bf16x8*>(a);
;         bf16x8 b1 = *reinterpret_cast<const bf16x8*>(a + 32 * 256);
;         p0 = __builtin_amdgcn_mfma_f32_32x32x16_bf16(b0, qr[d0], p0, 0, 0, 0);
;         p1 = __builtin_amdgcn_mfma_f32_32x32x16_bf16(b1, qr[d0], p1, 0, 0, 0); }
;     if (EXT) { const char* xa = lds + OFF_X + KB * SHM_X + r32 * 32 + hi * 16;
;         bf16x8 x0 = *reinterpret_cast<const bf16x8*>(xa), x1 = *reinterpret_cast<const bf16x8*>(xa + 32 * 32);
;         p0 = __builtin_amdgcn_mfma_f32_32x32x16_bf16(x0, qx, p0, 0, 0, 0);
;         p1 = __builtin_amdgcn_mfma_f32_32x32x16_bf16(x1, qx, p1, 0, 0, 0); }
; template <int MODE> ...
;     ...
;     const unsigned mo = (unsigned)(qlo + r32) * 1024u;
;     ...
;     float m_reg = -1e30f, l_reg = 0.f; f32x16 o[4] = {};
;     ...
;     __syncthreads();
;     if constexpr (MODE == 0) {
;     ...
;         unsigned long long mw;
;         f32x16 pA0, pA1, pB0, pB1; float mnA = 0.f, mnB = 0.f, alA = 1.f, alB = 1.f; bf16x8 pa0, pa1, pa2, pa3;
;         const int NTr = je - jb;
;         KDMA(jb * KVBLK, 0); VM_WAIT(); __syncthreads();
;         mw = MLOAD(jb); KDMA((jb + 1) * KVBLK, 1); VDMA(jb * KVBLK, 0);
;         if (ACT(jb)) { qkt<0, false>(pA0, pA1, lds, r32, hi, qr, qx); mask_bits(pA0, pA1, mw, hi); partialSM(pA0, pA1, m_reg, mnA, alA); }
	s_add_i32 s64, s63, 0x8000
	s_mov_b32 s0, m0
	s_mov_b32 m0, s64
	s_nop 0
	global_load_lds_dwordx4 v204, s[6:7]
	s_mov_b32 m0, s0
	v_and_or_b32 v205, v2, s51, v3
	s_add_i32 s65, s63, 0xa000
	s_mov_b32 s0, m0
	s_mov_b32 m0, s65
	s_nop 0
	global_load_lds_dwordx4 v205, s[6:7]
	s_mov_b32 m0, s0
	s_lshl_b32 s0, s61, 3
	s_add_u32 s24, s37, s0
	s_addc_u32 s25, s38, 0
	s_waitcnt vmcnt(0)
	s_barrier
	global_load_dwordx2 v[34:35], v178, s[24:25]
	v_lshlrev_b32_e32 v36, 3, v192
	v_ashrrev_i32_e32 v5, 4, v86
	v_and_b32_e32 v37, 24, v36
	v_bfe_u32 v3, v86, 2, 2
	v_lshrrev_b32_e32 v4, 1, v86
	s_movk_i32 s1, 0x60
	v_and_b32_e32 v6, 0xfffff0, v5
	v_lshrrev_b32_e32 v5, 1, v5
	v_and_or_b32 v3, v4, 8, v3
	v_and_or_b32 v4, v86, s1, v37
	v_and_b32_e32 v5, 4, v5
	v_lshlrev_b32_e32 v4, 1, v4
	v_or3_b32 v5, v6, v5, v3
	v_ashrrev_i32_e32 v2, 8, v2
	s_add_u32 s6, s6, 0x4000
	v_lshl_or_b32 v196, v5, 8, v4
	v_and_b32_e32 v5, 0xfffff0, v2
	v_lshrrev_b32_e32 v2, 1, v2
	s_addc_u32 s7, s7, 0
	s_add_i32 s66, s63, 0xc000
	s_mov_b32 s1, m0
	s_mov_b32 m0, s66
	s_nop 0
	global_load_lds_dwordx4 v204, s[6:7]
	s_mov_b32 m0, s1
	s_add_i32 s67, s63, 0xe000
	v_and_b32_e32 v2, 4, v2
	s_mov_b32 s1, m0
	s_mov_b32 m0, s67
	s_nop 0
	global_load_lds_dwordx4 v205, s[6:7]
	s_mov_b32 m0, s1
	s_add_u32 s6, s20, s73
	v_or3_b32 v2, v5, v2, v3
	s_addc_u32 s7, s21, 0
	s_mov_b32 s1, m0
	s_mov_b32 m0, s63
	s_nop 0
	global_load_lds_dwordx4 v196, s[6:7]
	s_mov_b32 m0, s1
	v_lshl_or_b32 v197, v2, 8, v4
	s_add_i32 s68, s63, 0x2000
	s_mov_b32 s1, m0
	s_mov_b32 m0, s68
	s_nop 0
	global_load_lds_dwordx4 v197, s[6:7]
	s_mov_b32 m0, s1
	s_cmp_gt_u32 s61, s60
	s_cbranch_scc1 .LBB0_1157
	v_add3_u32 v42, 0, v202, v198
	ds_read_b128 v[2:5], v42 offset:32768
	ds_read_b128 v[18:21], v42 offset:40960
	v_bitop3_b32 v22, v203, v199, s50 bitop3:0x78
	v_add3_u32 v43, 0, v22, v198
	ds_read_b128 v[38:41], v43 offset:32768
	v_bitop3_b32 v44, v201, v199, s50 bitop3:0x78
	v_add3_u32 v44, 0, v44, v198
	v_bitop3_b32 v45, v200, v199, s50 bitop3:0x78
	v_add3_u32 v45, 0, v45, v198
	s_waitcnt lgkmcnt(2)
	v_mfma_f32_32x32x16_bf16 v[2:17], v[2:5], v[146:149], 0
	s_waitcnt vmcnt(0)
	v_lshrrev_b32_e32 v34, v193, v34
	v_lshrrev_b32_e32 v35, v193, v35
	s_waitcnt lgkmcnt(0)
	v_mfma_f32_32x32x16_bf16 v[2:17], v[38:41], v[150:153], v[2:17]
	ds_read_b128 v[38:41], v43 offset:40960
	v_mfma_f32_32x32x16_bf16 v[18:33], v[18:21], v[146:149], 0
	s_waitcnt lgkmcnt(0)
	v_mfma_f32_32x32x16_bf16 v[18:33], v[38:41], v[150:153], v[18:33]
	ds_read_b128 v[38:41], v44 offset:32768
	s_waitcnt lgkmcnt(0)
	v_mfma_f32_32x32x16_bf16 v[2:17], v[38:41], v[154:157], v[2:17]
	ds_read_b128 v[38:41], v44 offset:40960
	s_waitcnt lgkmcnt(0)
	v_mfma_f32_32x32x16_bf16 v[18:33], v[38:41], v[154:157], v[18:33]
	ds_read_b128 v[38:41], v45 offset:32768
	s_waitcnt lgkmcnt(0)
	v_mfma_f32_32x32x16_bf16 v[2:17], v[38:41], v[158:161], v[2:17]
	ds_read_b128 v[38:41], v45 offset:40960
	s_waitcnt lgkmcnt(0)
	v_mfma_f32_32x32x16_bf16 v[18:33], v[38:41], v[158:161], v[18:33]
	v_xor_b32_e32 v242, 0x80, v42
	v_xor_b32_e32 v243, 0x80, v43
	v_xor_b32_e32 v244, 0x80, v44
	v_xor_b32_e32 v245, 0x80, v45
	ds_read_b128 v[38:41], v242 offset:32768
	s_waitcnt lgkmcnt(0)
	v_mfma_f32_32x32x16_bf16 v[2:17], v[38:41], v[142:145], v[2:17]
	ds_read_b128 v[38:41], v242 offset:40960
	v_bfe_i32 v42, v34, 0, 1
	s_waitcnt lgkmcnt(0)
	v_mfma_f32_32x32x16_bf16 v[18:33], v[38:41], v[142:145], v[18:33]
	ds_read_b128 v[38:41], v243 offset:32768
	s_waitcnt lgkmcnt(0)
	v_mfma_f32_32x32x16_bf16 v[2:17], v[38:41], v[138:141], v[2:17]
	ds_read_b128 v[38:41], v243 offset:40960
	v_bfe_i32 v43, v35, 0, 1
	s_waitcnt lgkmcnt(0)
	v_mfma_f32_32x32x16_bf16 v[18:33], v[38:41], v[138:141], v[18:33]
	ds_read_b128 v[38:41], v244 offset:32768
	s_waitcnt lgkmcnt(0)
	v_mfma_f32_32x32x16_bf16 v[2:17], v[38:41], v[134:137], v[2:17]
	ds_read_b128 v[38:41], v244 offset:40960
	s_waitcnt lgkmcnt(0)
	v_mfma_f32_32x32x16_bf16 v[18:33], v[38:41], v[134:137], v[18:33]
	ds_read_b128 v[38:41], v245 offset:32768
	s_waitcnt lgkmcnt(0)
	v_mfma_f32_32x32x16_bf16 v[2:17], v[38:41], v[130:133], v[2:17]
	ds_read_b128 v[38:41], v245 offset:40960
	s_waitcnt lgkmcnt(0)
; __device__ __forceinline__ void mask_bits(f32x16& p0, f32x16& p1, unsigned long long mw, int hi) {
;     const unsigned lo = (unsigned)mw >> (4 * hi), hw = (unsigned)(mw >> 32) >> (4 * hi);
; #pragma unroll
;     for (int r = 0; r < 16; ++r) { const int c = (r & 3) + 8 * (r >> 2);
;         const unsigned t0 = (unsigned)((int)(lo << (31 - c)) >> 31), t1 = (unsigned)((int)(hw << (31 - c)) >> 31);
;         p0[r] = __uint_as_float(__builtin_amdgcn_bitop3_b32(__float_as_uint(p0[r]), 0xFF800000u, t0, 0xe4));
;         p1[r] = __uint_as_float(__builtin_amdgcn_bitop3_b32(__float_as_uint(p1[r]), 0xFF800000u, t1, 0xe4)); }
; }
; __device__ __forceinline__ void partialSM(f32x16& p0, f32x16& p1, float& m_reg, float& mn, float& alpha) {
;     float pmax = p0[0]; for (int r = 1; r < 16; ++r) pmax = fmaxf(pmax, p0[r]); for (int r = 0; r < 16; ++r) pmax = fmaxf(pmax, p1[r]);
;     { auto rr = __builtin_amdgcn_permlane32_swap(__float_as_uint(pmax), __float_as_uint(pmax), false, false);
;       pmax = fmaxf(__uint_as_float(rr[0]), __uint_as_float(rr[1])); }
;     constexpr float C2 = 1.4426950408889634f * SCALE;
;     if (__builtin_expect(__all((pmax - m_reg) * SCALE <= THR), 1)) { mn = m_reg; alpha = 1.f; }
;     else { mn = fmaxf(m_reg, pmax); alpha = __builtin_amdgcn_exp2f((m_reg - mn) * C2); m_reg = mn; }
;     const float mnL = -mn * C2;
;     for (int r = 0; r < 16; ++r) p0[r] = fmaf(p0[r], C2, mnL); for (int r = 0; r < 16; ++r) p1[r] = fmaf(p1[r], C2, mnL);
;     for (int r = 0; r < 16; ++r) p0[r] = __builtin_amdgcn_exp2f(p0[r]);
; }
	v_mfma_f32_32x32x16_bf16 v[18:33], v[38:41], v[130:133], v[18:33]
	s_nop 8
	v_bitop3_b32 v42, v2, s52, v42 bitop3:0xe4
	v_bfe_i32 v38, v35, 1, 1
	s_nop 0
	v_bitop3_b32 v2, v18, s52, v43 bitop3:0xe4
	v_bfe_i32 v18, v34, 1, 1
	v_bitop3_b32 v39, v3, s52, v18 bitop3:0xe4
	v_bitop3_b32 v3, v19, s52, v38 bitop3:0xe4
	v_bfe_i32 v18, v34, 2, 1
	v_bfe_i32 v19, v35, 2, 1
	v_bitop3_b32 v38, v4, s52, v18 bitop3:0xe4
	v_bitop3_b32 v4, v20, s52, v19 bitop3:0xe4
	v_bfe_i32 v18, v34, 3, 1
	v_bfe_i32 v19, v35, 3, 1
	v_bitop3_b32 v20, v5, s52, v18 bitop3:0xe4
	v_bitop3_b32 v5, v21, s52, v19 bitop3:0xe4
	v_bfe_i32 v18, v34, 8, 1
	v_bfe_i32 v19, v35, 8, 1
	v_bitop3_b32 v21, v6, s52, v18 bitop3:0xe4
	v_bitop3_b32 v6, v22, s52, v19 bitop3:0xe4
	v_bfe_i32 v18, v34, 9, 1
	v_bfe_i32 v19, v35, 9, 1
	v_bitop3_b32 v22, v7, s52, v18 bitop3:0xe4
	v_bitop3_b32 v7, v23, s52, v19 bitop3:0xe4
	v_bfe_i32 v18, v34, 10, 1
	v_bfe_i32 v19, v35, 10, 1
	v_bitop3_b32 v23, v8, s52, v18 bitop3:0xe4
	v_bitop3_b32 v8, v24, s52, v19 bitop3:0xe4
	v_bfe_i32 v18, v34, 11, 1
	v_bfe_i32 v19, v35, 11, 1
	v_bitop3_b32 v24, v9, s52, v18 bitop3:0xe4
	v_bitop3_b32 v9, v25, s52, v19 bitop3:0xe4
	v_bfe_i32 v18, v34, 16, 1
	v_bfe_i32 v19, v35, 16, 1
	v_bitop3_b32 v25, v10, s52, v18 bitop3:0xe4
	v_bitop3_b32 v10, v26, s52, v19 bitop3:0xe4
	v_bfe_i32 v18, v34, 17, 1
	v_bfe_i32 v19, v35, 17, 1
	v_bitop3_b32 v26, v11, s52, v18 bitop3:0xe4
	v_bitop3_b32 v11, v27, s52, v19 bitop3:0xe4
	v_bfe_i32 v18, v34, 18, 1
	v_bfe_i32 v19, v35, 18, 1
	v_bitop3_b32 v27, v12, s52, v18 bitop3:0xe4
	v_bitop3_b32 v12, v28, s52, v19 bitop3:0xe4
	v_bfe_i32 v18, v34, 19, 1
	v_bfe_i32 v19, v35, 19, 1
	v_bitop3_b32 v28, v13, s52, v18 bitop3:0xe4
	v_bitop3_b32 v13, v29, s52, v19 bitop3:0xe4
	v_bfe_i32 v18, v34, 24, 1
	v_bfe_i32 v19, v35, 24, 1
	v_bitop3_b32 v29, v14, s52, v18 bitop3:0xe4
	v_bitop3_b32 v14, v30, s52, v19 bitop3:0xe4
	v_bfe_i32 v18, v34, 25, 1
	v_bfe_i32 v19, v35, 25, 1
	v_bitop3_b32 v30, v15, s52, v18 bitop3:0xe4
	v_bitop3_b32 v15, v31, s52, v19 bitop3:0xe4
	v_bfe_i32 v18, v34, 26, 1
	v_bfe_i32 v19, v35, 26, 1
	v_bitop3_b32 v31, v16, s52, v18 bitop3:0xe4
	v_bitop3_b32 v16, v32, s52, v19 bitop3:0xe4
	v_bfe_i32 v18, v34, 27, 1
	v_bfe_i32 v19, v35, 27, 1
	v_bitop3_b32 v32, v17, s52, v18 bitop3:0xe4
	v_bitop3_b32 v17, v33, s52, v19 bitop3:0xe4
	v_max_f32_e32 v18, v39, v39
	v_max_f32_e32 v19, v42, v42
	v_max_f32_e32 v18, v19, v18
	v_max3_f32 v18, v18, v38, v20
	v_max3_f32 v18, v18, v21, v22
	v_max3_f32 v18, v18, v23, v24
	v_max3_f32 v18, v18, v25, v26
	v_max3_f32 v18, v18, v27, v28
	v_max3_f32 v18, v18, v29, v30
	v_max3_f32 v18, v18, v31, v32
	v_max3_f32 v18, v18, v2, v3
	v_max3_f32 v18, v18, v4, v5
	v_max3_f32 v18, v18, v6, v7
	v_max3_f32 v18, v18, v8, v9
	v_max3_f32 v18, v18, v10, v11
	v_max3_f32 v18, v18, v12, v13
	v_max3_f32 v18, v18, v14, v15
	v_max3_f32 v18, v18, v16, v17
	v_mov_b32_e32 v19, v18
	s_nop 1
	v_permlane32_swap_b32_e32 v18, v19
	v_max_f32_e32 v19, v19, v19
	v_max_f32_e32 v18, v18, v18
	v_max_f32_e32 v18, v18, v19
	v_add_f32_e32 v19, 0x7149f2ca, v18
	v_mul_f32_e32 v19, 0x3db504f3, v19
	v_max_f32_e32 v18, 0xf149f2ca, v18
	v_cmp_ge_f32_e32 vcc, s53, v19
	v_sub_f32_e32 v19, 0xf149f2ca, v18
	v_mul_f32_e32 v19, 0x3e0293ee, v19
	s_cmp_eq_u64 vcc, exec
	v_exp_f32_e32 v19, v19
	s_cselect_b64 vcc, -1, 0
	v_cndmask_b32_e32 v180, v18, v189, vcc
	v_mul_f32_e32 v18, 0xbe0293ee, v180
	v_mov_b32_e32 v35, v18
	v_cndmask_b32_e64 v206, v19, 1.0, vcc
	v_fmamk_f32 v19, v42, 0x3e0293ee, v18
	v_fmamk_f32 v33, v39, 0x3e0293ee, v18
	v_fmamk_f32 v34, v38, 0x3e0293ee, v18
	v_fmamk_f32 v20, v20, 0x3e0293ee, v18
	v_fmamk_f32 v21, v21, 0x3e0293ee, v18
	v_fmamk_f32 v22, v22, 0x3e0293ee, v18
	v_fmamk_f32 v23, v23, 0x3e0293ee, v18
	v_fmamk_f32 v24, v24, 0x3e0293ee, v18
	v_fmamk_f32 v25, v25, 0x3e0293ee, v18
	v_fmamk_f32 v26, v26, 0x3e0293ee, v18
	v_fmamk_f32 v27, v27, 0x3e0293ee, v18
	v_fmamk_f32 v28, v28, 0x3e0293ee, v18
	v_fmamk_f32 v29, v29, 0x3e0293ee, v18
	v_fmamk_f32 v30, v30, 0x3e0293ee, v18
	v_fmamk_f32 v31, v31, 0x3e0293ee, v18
	v_fmac_f32_e32 v35, 0x3e0293ee, v32
	v_exp_f32_e32 v98, v19
	v_exp_f32_e32 v99, v33
	v_exp_f32_e32 v100, v34
	v_exp_f32_e32 v101, v20
	v_exp_f32_e32 v102, v21
	v_exp_f32_e32 v103, v22
	v_exp_f32_e32 v104, v23
	v_exp_f32_e32 v105, v24
	v_exp_f32_e32 v106, v25
	v_exp_f32_e32 v107, v26
	v_exp_f32_e32 v108, v27
	v_exp_f32_e32 v109, v28
	v_exp_f32_e32 v110, v29
	v_exp_f32_e32 v111, v30
	v_exp_f32_e32 v112, v31
	v_exp_f32_e32 v113, v35
	v_pk_fma_f32 v[128:129], v[16:17], s[12:13], v[18:19] op_sel_hi:[1,0,0]
	v_pk_fma_f32 v[126:127], v[14:15], s[12:13], v[18:19] op_sel_hi:[1,0,0]
	v_pk_fma_f32 v[124:125], v[12:13], s[12:13], v[18:19] op_sel_hi:[1,0,0]
	v_pk_fma_f32 v[122:123], v[10:11], s[12:13], v[18:19] op_sel_hi:[1,0,0]
	v_pk_fma_f32 v[120:121], v[8:9], s[12:13], v[18:19] op_sel_hi:[1,0,0]
	v_pk_fma_f32 v[118:119], v[6:7], s[12:13], v[18:19] op_sel_hi:[1,0,0]
	v_pk_fma_f32 v[116:117], v[4:5], s[12:13], v[18:19] op_sel_hi:[1,0,0]
	v_pk_fma_f32 v[114:115], v[2:3], s[12:13], v[18:19] op_sel_hi:[1,0,0]
	s_branch .LBB0_1158

; template <int KB, bool EXT>
; __device__ __forceinline__ void qkt(f32x16& p0, f32x16& p1, const char* lds, int r32, int hi, const bf16x8* qr, bf16x8 qx) {
;     ...
;     for (int dd = 0; dd < 4; ++dd) kb[dd] = lds + OFF_K + KB * SHM_K + KSWZ(r32, (dd * 16 + hi * 8) * 2);
; #pragma unroll
;     for (int d0 = 0; d0 < 8; ++d0) { const char* a = kb[d0 & 3] + (d0 >> 2) * 128;
;         bf16x8 b0 = *reinterpret_cast<const bf16x8*>(a);
;         bf16x8 b1 = *reinterpret_cast<const bf16x8*>(a + 32 * 256);
;         p0 = __builtin_amdgcn_mfma_f32_32x32x16_bf16(b0, qr[d0], p0, 0, 0, 0);
;         p1 = __builtin_amdgcn_mfma_f32_32x32x16_bf16(b1, qr[d0], p1, 0, 0, 0); }
; template <int MODE> ...
;     ...
;         const int tdiag = P0 / KVBLK; int r = 1;
;         for (; r + 1 < NTr && jb + r + 1 <= tdiag; r += 2) {
;             HALFU(pB0, pB1, mnB, alB, pA0, pA1, alA, jb + r, 1, 0);
;             HALFU(pA0, pA1, mnA, alA, pB0, pB1, alB, jb + r + 1, 0, 1);
.LBB0_1158:
	s_cmp_eq_u32 s58, 1
	s_cselect_b32 s69, s3, s2
	s_lshl_b32 s1, s4, 2
	s_add_i32 s62, s1, 0
	s_add_i32 s62, s62, 0x11000
	v_lshlrev_b32_e32 v3, 1, v192
	v_lshlrev_b32_e32 v2, 4, v192
	v_and_b32_e32 v3, 32, v3
	s_movk_i32 s1, 0xc0
	s_cmp_lg_u32 0, -1
	v_and_or_b32 v2, v2, s1, v3
	s_cselect_b32 s1, 0, 0
	v_and_b32_e32 v3, 0x100, v36
	s_sub_i32 s2, s69, s61
	s_waitcnt vmcnt(0)
	s_add_i32 s33, s1, s72
	v_or3_b32 v2, v2, v3, v37
	s_add_i32 s70, s2, -1
	s_addk_i32 s33, 0x4000
	s_mov_b32 s26, 1
	v_add_u32_e32 v194, s1, v2
	s_cmp_lt_i32 s2, 3
	s_barrier
	s_cbranch_scc1 .LBB0_1175
	s_or_b32 s1, s61, 1
	s_cmp_ge_u32 s1, s71
	s_mov_b32 s74, 0
	s_cbranch_scc1 .LBB0_1177
	s_cmp_lg_u32 0, -1
	s_cselect_b32 s1, 0, 0
	s_add_i32 s1, s1, s72
	v_and_b32_e32 v2, 0xf0, v199
	s_add_i32 s75, s1, 0x6000
	v_xad_u32 v18, v2, v207, 0
	v_xad_u32 v19, v203, v2, 0
	v_xad_u32 v20, v201, v2, 0
	v_xad_u32 v21, v200, v2, 0
	s_add_u32 s0, s45, s0
	v_mov_b32_e32 v16, v179
	v_mov_b32_e32 v17, v179
	s_addc_u32 s1, s46, 0
	v_mov_b32_e32 v2, v179
	v_mov_b32_e32 v3, v179
	v_mov_b32_e32 v4, v179
	v_mov_b32_e32 v5, v179
	v_mov_b32_e32 v6, v179
	v_mov_b32_e32 v7, v179
	v_mov_b32_e32 v8, v179
	v_mov_b32_e32 v9, v179
	v_mov_b32_e32 v10, v179
	v_mov_b32_e32 v11, v179
	v_mov_b32_e32 v12, v179
	v_mov_b32_e32 v13, v179
	v_mov_b32_e32 v14, v179
	v_mov_b32_e32 v15, v179
	v_add_u32_e32 v210, v18, v198
	v_add_u32_e32 v211, v19, v198
	v_add_u32_e32 v212, v20, v198
	v_add_u32_e32 v213, v21, v198
	v_mov_b64_e32 v[64:65], v[16:17]
	s_waitcnt vmcnt(0)
	v_mov_b64_e32 v[48:49], v[16:17]
	v_mov_b64_e32 v[32:33], v[16:17]
	v_cmp_gt_u32_e64 s[2:3], 32, v192
	v_lshl_add_u32 v208, v190, 2, s62
	v_add_u32_e32 v209, s62, v207
	v_lshl_add_u64 v[182:183], s[0:1], 0, v[178:179]
	v_mov_b32_e32 v181, 0
	s_mov_b64 s[0:1], s[18:19]
	s_mov_b64 s[6:7], s[20:21]
	v_mov_b32_e32 v214, v206
	v_mov_b64_e32 v[62:63], v[14:15]
	v_mov_b64_e32 v[60:61], v[12:13]
	v_mov_b64_e32 v[58:59], v[10:11]
	v_mov_b64_e32 v[56:57], v[8:9]
	v_mov_b64_e32 v[54:55], v[6:7]
	v_mov_b64_e32 v[52:53], v[4:5]
	v_mov_b64_e32 v[50:51], v[2:3]
	v_mov_b64_e32 v[46:47], v[14:15]
	v_mov_b64_e32 v[44:45], v[12:13]
	v_mov_b64_e32 v[42:43], v[10:11]
	v_mov_b64_e32 v[40:41], v[8:9]
	v_mov_b64_e32 v[38:39], v[6:7]
	v_mov_b64_e32 v[36:37], v[4:5]
	v_mov_b64_e32 v[34:35], v[2:3]
	v_mov_b64_e32 v[30:31], v[14:15]
	v_mov_b64_e32 v[28:29], v[12:13]
	v_mov_b64_e32 v[26:27], v[10:11]
	v_mov_b64_e32 v[24:25], v[8:9]
	v_mov_b64_e32 v[22:23], v[6:7]
	v_mov_b64_e32 v[20:21], v[4:5]
	v_mov_b64_e32 v[18:19], v[2:3]
	v_readfirstlane_b32 s99, v0
	s_nop 0
	s_lshr_b32 s99, s99, 8
.LBB0_1161:
	global_load_dwordx2 v[162:163], v[182:183], off offset:-8
	s_add_u32 s76, s0, s73
	s_addc_u32 s77, s1, 0
	s_add_u32 s4, s76, 0x8000
	s_addc_u32 s5, s77, 0
	s_add_u32 s26, s6, s73
	s_mov_b32 s24, m0
	s_mov_b32 m0, s64
	s_nop 0
	global_load_lds_dwordx4 v204, s[4:5]
	s_mov_b32 m0, s24
	s_addc_u32 s27, s7, 0
	s_mov_b32 s24, m0
	s_mov_b32 m0, s65
	s_nop 0
	global_load_lds_dwordx4 v205, s[4:5]
	s_mov_b32 m0, s24
	s_add_u32 s4, s26, 0x4000
	s_addc_u32 s5, s27, 0
	s_mov_b32 s24, m0
	s_mov_b32 m0, s33
	s_nop 0
	global_load_lds_dwordx4 v196, s[4:5]
	s_mov_b32 m0, s24
	s_nop 0
	s_mov_b32 s24, m0
	s_mov_b32 m0, s75
	s_nop 0
	global_load_lds_dwordx4 v197, s[4:5]
	s_mov_b32 m0, s24
	ds_read_b128 v[66:69], v210 offset:49152
	ds_read_b128 v[82:85], v210 offset:57344
	ds_read_b128 v[164:167], v211 offset:49152
	ds_read_b128 v[168:171], v211 offset:57344
	ds_read_b128 v[246:249], v212 offset:49152
	ds_read_b128 v[250:253], v212 offset:57344
	v_exp_f32_e32 v114, v114
	v_exp_f32_e32 v115, v115
	s_waitcnt lgkmcnt(5)
	v_mfma_f32_32x32x16_bf16 v[66:81], v[66:69], v[146:149], 0
	v_exp_f32_e32 v116, v116
	v_exp_f32_e32 v117, v117
	v_exp_f32_e32 v118, v118
	v_exp_f32_e32 v119, v119
	v_exp_f32_e32 v120, v120
	v_exp_f32_e32 v121, v121
	v_exp_f32_e32 v122, v122
	s_waitcnt lgkmcnt(4)
	v_mfma_f32_32x32x16_bf16 v[82:97], v[82:85], v[146:149], 0
	v_exp_f32_e32 v123, v123
	v_exp_f32_e32 v124, v124
	v_exp_f32_e32 v125, v125
	v_exp_f32_e32 v126, v126
	v_exp_f32_e32 v127, v127
	v_exp_f32_e32 v128, v128
	v_exp_f32_e32 v129, v129
	s_waitcnt lgkmcnt(3)
	v_mfma_f32_32x32x16_bf16 v[66:81], v[164:167], v[150:153], v[66:81]
	ds_read_b128 v[164:167], v213 offset:49152
	s_waitcnt lgkmcnt(3)
	v_mfma_f32_32x32x16_bf16 v[82:97], v[168:171], v[150:153], v[82:97]
	ds_read_b128 v[168:171], v213 offset:57344
	s_waitcnt lgkmcnt(3)
	v_mfma_f32_32x32x16_bf16 v[66:81], v[246:249], v[154:157], v[66:81]
	ds_read_b128 v[246:249], v242 offset:49152
	s_waitcnt lgkmcnt(3)
	v_mfma_f32_32x32x16_bf16 v[82:97], v[250:253], v[154:157], v[82:97]
	ds_read_b128 v[250:253], v242 offset:57344
	s_waitcnt lgkmcnt(3)
	v_mfma_f32_32x32x16_bf16 v[66:81], v[164:167], v[158:161], v[66:81]
	ds_read_b128 v[164:167], v243 offset:49152
	s_waitcnt lgkmcnt(3)
	v_mfma_f32_32x32x16_bf16 v[82:97], v[168:171], v[158:161], v[82:97]
	ds_read_b128 v[168:171], v243 offset:57344
	v_xor_b32_e32 v242, 0x80, v210
	v_xor_b32_e32 v243, 0x80, v211
	v_xor_b32_e32 v244, 0x80, v212
	v_xor_b32_e32 v245, 0x80, v213
	s_waitcnt lgkmcnt(3)
	v_mfma_f32_32x32x16_bf16 v[66:81], v[246:249], v[142:145], v[66:81]
	ds_read_b128 v[246:249], v244 offset:49152
	s_waitcnt lgkmcnt(3)
	v_mfma_f32_32x32x16_bf16 v[82:97], v[250:253], v[142:145], v[82:97]
	ds_read_b128 v[250:253], v244 offset:57344
	s_waitcnt lgkmcnt(3)
; __device__ __forceinline__ void finishSM(f32x16& p0, f32x16& p1, float alpha, float& l_reg, bf16x8& pa0, bf16x8& pa1, bf16x8& pa2, bf16x8& pa3) {
;     for (int r = 0; r < 16; ++r) p1[r] = __builtin_amdgcn_exp2f(p1[r]);
;     float ps = 0; for (int r = 0; r < 16; ++r) ps += p0[r]; for (int r = 0; r < 16; ++r) ps += p1[r];
;     { auto rr = __builtin_amdgcn_permlane32_swap(__float_as_uint(ps), __float_as_uint(ps), false, false);
;       ps = __uint_as_float(rr[0]) + __uint_as_float(rr[1]); }
;     l_reg = l_reg * alpha + ps;
;     ...
;     PK4(p0, 0, pa0); PK4(p0, 8, pa1); PK4(p1, 0, pa2); PK4(p1, 8, pa3);
;     ...
; }
; template <int KB, bool EXT>
; __device__ __forceinline__ void qkt(f32x16& p0, f32x16& p1, const char* lds, int r32, int hi, const bf16x8* qr, bf16x8 qx) {
;     p0 = f32x16{}; p1 = f32x16{};
;     const char* kb[4];
; #pragma unroll
;     for (int dd = 0; dd < 4; ++dd) kb[dd] = lds + OFF_K + KB * SHM_K + KSWZ(r32, (dd * 16 + hi * 8) * 2);
; #pragma unroll
;     for (int d0 = 0; d0 < 8; ++d0) { const char* a = kb[d0 & 3] + (d0 >> 2) * 128;
;         bf16x8 b0 = *reinterpret_cast<const bf16x8*>(a);
;         bf16x8 b1 = *reinterpret_cast<const bf16x8*>(a + 32 * 256);
;         p0 = __builtin_amdgcn_mfma_f32_32x32x16_bf16(b0, qr[d0], p0, 0, 0, 0);
;         p1 = __builtin_amdgcn_mfma_f32_32x32x16_bf16(b1, qr[d0], p1, 0, 0, 0); }
;     if (EXT) { const char* xa = lds + OFF_X + KB * SHM_X + r32 * 32 + hi * 16;
;         bf16x8 x0 = *reinterpret_cast<const bf16x8*>(xa), x1 = *reinterpret_cast<const bf16x8*>(xa + 32 * 32);
;         p0 = __builtin_amdgcn_mfma_f32_32x32x16_bf16(x0, qx, p0, 0, 0, 0);
;         p1 = __builtin_amdgcn_mfma_f32_32x32x16_bf16(x1, qx, p1, 0, 0, 0); }
; }
; template <int VB>
; __device__ __forceinline__ void pv_tile(f32x16* o, int vb0, bf16x8 pa0, bf16x8 pa1, bf16x8 pa2, bf16x8 pa3) {
;     ...
;     PV_D0(0); PV_D0(1); PV_D0(2); PV_D0(3);
	v_mfma_f32_32x32x16_bf16 v[66:81], v[164:167], v[138:141], v[66:81]
	ds_read_b128 v[164:167], v245 offset:49152
	s_waitcnt lgkmcnt(3)
	v_mfma_f32_32x32x16_bf16 v[82:97], v[168:171], v[138:141], v[82:97]
	ds_read_b128 v[168:171], v245 offset:57344
	s_waitcnt lgkmcnt(3)
	v_mfma_f32_32x32x16_bf16 v[66:81], v[246:249], v[134:137], v[66:81]
	s_waitcnt lgkmcnt(2)
	v_mfma_f32_32x32x16_bf16 v[82:97], v[250:253], v[134:137], v[82:97]
	s_waitcnt lgkmcnt(1)
	v_mfma_f32_32x32x16_bf16 v[66:81], v[164:167], v[130:133], v[66:81]
	v_add_f32_e32 v164, 0, v98
	v_add_f32_e32 v164, v99, v164
	v_add_f32_e32 v164, v100, v164
	v_add_f32_e32 v164, v101, v164
	v_add_f32_e32 v164, v102, v164
	v_add_f32_e32 v164, v103, v164
	v_add_f32_e32 v164, v104, v164
	v_add_f32_e32 v164, v105, v164
	v_add_f32_e32 v164, v106, v164
	v_add_f32_e32 v164, v107, v164
	v_add_f32_e32 v164, v108, v164
	v_add_f32_e32 v164, v109, v164
	v_add_f32_e32 v164, v110, v164
	v_add_f32_e32 v164, v111, v164
	v_add_f32_e32 v164, v112, v164
	v_add_f32_e32 v164, v113, v164
	v_add_f32_e32 v164, v114, v164
	v_add_f32_e32 v164, v115, v164
	v_add_f32_e32 v164, v116, v164
	v_add_f32_e32 v164, v117, v164
	v_add_f32_e32 v164, v118, v164
	v_add_f32_e32 v164, v119, v164
	v_add_f32_e32 v164, v120, v164
	v_add_f32_e32 v164, v121, v164
	v_add_f32_e32 v164, v122, v164
	v_add_f32_e32 v164, v123, v164
	s_waitcnt lgkmcnt(0)
	v_mfma_f32_32x32x16_bf16 v[82:97], v[168:171], v[130:133], v[82:97]
	v_add_f32_e32 v164, v124, v164
	v_add_f32_e32 v164, v125, v164
	v_add_f32_e32 v164, v126, v164
	v_add_f32_e32 v164, v127, v164
	v_add_f32_e32 v164, v128, v164
	v_add_f32_e32 v215, v129, v164
	v_mov_b32_e32 v216, v215
	v_cvt_pk_bf16_f32 v98, v98, v99
	v_cvt_pk_bf16_f32 v99, v100, v101
	v_cvt_pk_bf16_f32 v100, v102, v103
	s_nop 1
	v_permlane32_swap_b32_e32 v215, v216
	v_cvt_pk_bf16_f32 v101, v104, v105
	v_permlane32_swap_b32_e32 v98, v100
	v_cvt_pk_bf16_f32 v102, v106, v107
	v_cvt_pk_bf16_f32 v103, v108, v109
	v_cvt_pk_bf16_f32 v104, v110, v111
	v_cvt_pk_bf16_f32 v105, v112, v113
	v_cvt_pk_bf16_f32 v106, v114, v115
	v_cvt_pk_bf16_f32 v107, v116, v117
	v_cvt_pk_bf16_f32 v108, v118, v119
	v_cvt_pk_bf16_f32 v109, v120, v121
	v_cvt_pk_bf16_f32 v110, v122, v123
	v_cvt_pk_bf16_f32 v111, v124, v125
	v_cvt_pk_bf16_f32 v112, v126, v127
	v_cvt_pk_bf16_f32 v113, v128, v129
	v_permlane32_swap_b32_e32 v99, v101
	v_permlane32_swap_b32_e32 v102, v104
	v_permlane32_swap_b32_e32 v103, v105
	v_permlane32_swap_b32_e32 v106, v108
	v_permlane32_swap_b32_e32 v107, v109
	v_permlane32_swap_b32_e32 v110, v112
	v_permlane32_swap_b32_e32 v111, v113
	ds_read_b64_tr_b16 v[114:115], v194 offset:0
	ds_read_b64_tr_b16 v[116:117], v194 offset:0x800
	ds_read_b64_tr_b16 v[118:119], v194 offset:0x1000
	ds_read_b64_tr_b16 v[120:121], v194 offset:0x1800
	ds_read_b64_tr_b16 v[122:123], v194 offset:0x2000
	ds_read_b64_tr_b16 v[124:125], v194 offset:0x2800
	ds_read_b64_tr_b16 v[126:127], v194 offset:0x3000
	ds_read_b64_tr_b16 v[128:129], v194 offset:0x3800
	s_waitcnt lgkmcnt(0)
	s_nop 0
	v_mfma_f32_32x32x16_bf16 v[2:17], v[98:101], v[114:117], v[2:17]
	ds_read_b64_tr_b16 v[114:115], v194 offset:0x200
	ds_read_b64_tr_b16 v[116:117], v194 offset:0xa00
	v_mfma_f32_32x32x16_bf16 v[2:17], v[102:105], v[118:121], v[2:17]
	ds_read_b64_tr_b16 v[118:119], v194 offset:0x1200
	ds_read_b64_tr_b16 v[120:121], v194 offset:0x1a00
	v_mfma_f32_32x32x16_bf16 v[2:17], v[106:109], v[122:125], v[2:17]
	ds_read_b64_tr_b16 v[122:123], v194 offset:0x2200
	ds_read_b64_tr_b16 v[124:125], v194 offset:0x2a00
	v_mfma_f32_32x32x16_bf16 v[2:17], v[110:113], v[126:129], v[2:17]
	ds_read_b64_tr_b16 v[126:127], v194 offset:0x3200
	ds_read_b64_tr_b16 v[128:129], v194 offset:0x3a00
	s_waitcnt lgkmcnt(0)
	v_mfma_f32_32x32x16_bf16 v[50:65], v[98:101], v[114:117], v[50:65]
	ds_read_b64_tr_b16 v[114:115], v194 offset:0x400
	ds_read_b64_tr_b16 v[116:117], v194 offset:0xc00
	v_mfma_f32_32x32x16_bf16 v[50:65], v[102:105], v[118:121], v[50:65]
	ds_read_b64_tr_b16 v[118:119], v194 offset:0x1400
	ds_read_b64_tr_b16 v[120:121], v194 offset:0x1c00
	v_mfma_f32_32x32x16_bf16 v[50:65], v[106:109], v[122:125], v[50:65]
	ds_read_b64_tr_b16 v[122:123], v194 offset:0x2400
	ds_read_b64_tr_b16 v[124:125], v194 offset:0x2c00
	v_mfma_f32_32x32x16_bf16 v[50:65], v[110:113], v[126:129], v[50:65]
	ds_read_b64_tr_b16 v[126:127], v194 offset:0x3400
	ds_read_b64_tr_b16 v[128:129], v194 offset:0x3c00
	s_waitcnt lgkmcnt(0)
	v_mfma_f32_32x32x16_bf16 v[34:49], v[98:101], v[114:117], v[34:49]
	ds_read_b64_tr_b16 v[114:115], v194 offset:0x600
	ds_read_b64_tr_b16 v[116:117], v194 offset:0xe00
	v_mfma_f32_32x32x16_bf16 v[34:49], v[102:105], v[118:121], v[34:49]
	ds_read_b64_tr_b16 v[118:119], v194 offset:0x1600
	ds_read_b64_tr_b16 v[120:121], v194 offset:0x1e00
	v_mfma_f32_32x32x16_bf16 v[34:49], v[106:109], v[122:125], v[34:49]
	ds_read_b64_tr_b16 v[122:123], v194 offset:0x2600
	ds_read_b64_tr_b16 v[124:125], v194 offset:0x2e00
	v_mfma_f32_32x32x16_bf16 v[34:49], v[110:113], v[126:129], v[34:49]
	ds_read_b64_tr_b16 v[126:127], v194 offset:0x3600
	ds_read_b64_tr_b16 v[128:129], v194 offset:0x3e00
	s_waitcnt lgkmcnt(0)
	v_mfma_f32_32x32x16_bf16 v[18:33], v[98:101], v[114:117], v[18:33]
	s_waitcnt vmcnt(0)
	s_cmp_eq_u32 s99, 0
	s_cbranch_scc1 .Lstg_p1a
	s_barrier

; __device__ __forceinline__ void partialSM(f32x16& p0, f32x16& p1, float& m_reg, float& mn, float& alpha) {
;     ...
;     for (int r = 0; r < 16; ++r) p0[r] = fmaf(p0[r], C2, mnL); for (int r = 0; r < 16; ++r) p1[r] = fmaf(p1[r], C2, mnL);
;     for (int r = 0; r < 16; ++r) p0[r] = __builtin_amdgcn_exp2f(p0[r]);
; }
; __device__ __forceinline__ void finishSM(f32x16& p0, f32x16& p1, float alpha, float& l_reg, bf16x8& pa0, bf16x8& pa1, bf16x8& pa2, bf16x8& pa3) {
;     for (int r = 0; r < 16; ++r) p1[r] = __builtin_amdgcn_exp2f(p1[r]);
;     float ps = 0; for (int r = 0; r < 16; ++r) ps += p0[r]; for (int r = 0; r < 16; ++r) ps += p1[r];
;     { auto rr = __builtin_amdgcn_permlane32_swap(__float_as_uint(ps), __float_as_uint(ps), false, false);
;       ps = __uint_as_float(rr[0]) + __uint_as_float(rr[1]); }
;     l_reg = l_reg * alpha + ps;
;     ...
;     PK4(p0, 0, pa0); PK4(p0, 8, pa1); PK4(p1, 0, pa2); PK4(p1, 8, pa3);
;     ...
; }
; template <int KB, bool EXT>
; __device__ __forceinline__ void qkt(f32x16& p0, f32x16& p1, const char* lds, int r32, int hi, const bf16x8* qr, bf16x8 qx) {
;     p0 = f32x16{}; p1 = f32x16{};
;     const char* kb[4];
; #pragma unroll
;     for (int dd = 0; dd < 4; ++dd) kb[dd] = lds + OFF_K + KB * SHM_K + KSWZ(r32, (dd * 16 + hi * 8) * 2);
; #pragma unroll
;     for (int d0 = 0; d0 < 8; ++d0) { const char* a = kb[d0 & 3] + (d0 >> 2) * 128;
;         bf16x8 b0 = *reinterpret_cast<const bf16x8*>(a);
;         bf16x8 b1 = *reinterpret_cast<const bf16x8*>(a + 32 * 256);
;         p0 = __builtin_amdgcn_mfma_f32_32x32x16_bf16(b0, qr[d0], p0, 0, 0, 0);
;         p1 = __builtin_amdgcn_mfma_f32_32x32x16_bf16(b1, qr[d0], p1, 0, 0, 0); }
.LBB0_1167:
	v_cndmask_b32_e64 v180, v97, v180, s[4:5]
	v_mul_f32_e32 v97, 0xbe0293ee, v180
	v_fmamk_f32 v66, v66, 0x3e0293ee, v97
	v_fmamk_f32 v67, v67, 0x3e0293ee, v97
	v_fmamk_f32 v68, v68, 0x3e0293ee, v97
	v_fmamk_f32 v69, v69, 0x3e0293ee, v97
	v_fmamk_f32 v70, v70, 0x3e0293ee, v97
	v_fmamk_f32 v71, v71, 0x3e0293ee, v97
	v_fmamk_f32 v72, v72, 0x3e0293ee, v97
	v_fmamk_f32 v73, v73, 0x3e0293ee, v97
	v_fmamk_f32 v74, v74, 0x3e0293ee, v97
	v_fmamk_f32 v75, v75, 0x3e0293ee, v97
	v_fmamk_f32 v76, v76, 0x3e0293ee, v97
	v_fmamk_f32 v77, v77, 0x3e0293ee, v97
	v_fmamk_f32 v78, v78, 0x3e0293ee, v97
	v_fmamk_f32 v79, v79, 0x3e0293ee, v97
	v_fmamk_f32 v98, v98, 0x3e0293ee, v97
	v_fmamk_f32 v96, v96, 0x3e0293ee, v97
	s_add_u32 s4, s26, 0x8000
	v_fmamk_f32 v162, v82, 0x3e0293ee, v97
	v_fmamk_f32 v163, v83, 0x3e0293ee, v97
	v_fmamk_f32 v164, v84, 0x3e0293ee, v97
	v_fmamk_f32 v165, v85, 0x3e0293ee, v97
	v_fmamk_f32 v166, v86, 0x3e0293ee, v97
	v_fmamk_f32 v167, v87, 0x3e0293ee, v97
	v_fmamk_f32 v168, v88, 0x3e0293ee, v97
	v_fmamk_f32 v169, v89, 0x3e0293ee, v97
	v_fmamk_f32 v90, v90, 0x3e0293ee, v97
	v_fmamk_f32 v91, v91, 0x3e0293ee, v97
	v_fmamk_f32 v92, v92, 0x3e0293ee, v97
	v_fmamk_f32 v93, v93, 0x3e0293ee, v97
	v_fmamk_f32 v94, v94, 0x3e0293ee, v97
	v_fmamk_f32 v95, v95, 0x3e0293ee, v97
	v_fmamk_f32 v170, v80, 0x3e0293ee, v97
	v_fmac_f32_e32 v97, 0x3e0293ee, v81
	v_exp_f32_e32 v66, v66
	v_exp_f32_e32 v67, v67
	v_exp_f32_e32 v68, v68
	v_exp_f32_e32 v69, v69
	v_exp_f32_e32 v70, v70
	v_exp_f32_e32 v71, v71
	v_exp_f32_e32 v72, v72
	v_exp_f32_e32 v73, v73
	v_exp_f32_e32 v74, v74
	v_exp_f32_e32 v75, v75
	v_exp_f32_e32 v76, v76
	v_exp_f32_e32 v77, v77
	v_exp_f32_e32 v78, v78
	v_exp_f32_e32 v79, v79
	v_exp_f32_e32 v80, v98
	v_exp_f32_e32 v81, v96
	s_addc_u32 s5, s27, 0
	s_mov_b32 s24, m0
	s_mov_b32 m0, s63
	s_nop 0
	global_load_lds_dwordx4 v196, s[4:5]
	s_mov_b32 m0, s24
	s_nop 0
	s_mov_b32 s24, m0
	s_mov_b32 m0, s68
	s_nop 0
	global_load_lds_dwordx4 v197, s[4:5]
	s_mov_b32 m0, s24
	ds_read_b128 v[82:85], v210 offset:32768
	ds_read_b128 v[86:89], v210 offset:40960
	ds_read_b128 v[246:249], v211 offset:32768
	ds_read_b128 v[250:253], v211 offset:40960
	v_exp_f32_e32 v90, v90
	v_exp_f32_e32 v91, v91
	v_exp_f32_e32 v92, v92
	s_waitcnt lgkmcnt(3)
	v_mfma_f32_32x32x16_bf16 v[98:113], v[82:85], v[146:149], 0
	ds_read_b128 v[82:85], v212 offset:32768
	v_exp_f32_e32 v93, v93
	v_exp_f32_e32 v94, v94
	v_exp_f32_e32 v95, v95
	v_exp_f32_e32 v96, v170
	v_exp_f32_e32 v97, v97
	s_waitcnt lgkmcnt(3)
	v_mfma_f32_32x32x16_bf16 v[114:129], v[86:89], v[146:149], 0
	ds_read_b128 v[86:89], v212 offset:40960
	s_waitcnt lgkmcnt(3)
	v_mfma_f32_32x32x16_bf16 v[98:113], v[246:249], v[150:153], v[98:113]
	ds_read_b128 v[246:249], v213 offset:32768
	s_waitcnt lgkmcnt(3)
	v_mfma_f32_32x32x16_bf16 v[114:129], v[250:253], v[150:153], v[114:129]
	ds_read_b128 v[250:253], v213 offset:40960
	s_waitcnt lgkmcnt(3)
	v_mfma_f32_32x32x16_bf16 v[98:113], v[82:85], v[154:157], v[98:113]
	ds_read_b128 v[82:85], v242 offset:32768
	s_waitcnt lgkmcnt(3)
	v_mfma_f32_32x32x16_bf16 v[114:129], v[86:89], v[154:157], v[114:129]
	ds_read_b128 v[86:89], v242 offset:40960
	s_waitcnt lgkmcnt(3)
	v_mfma_f32_32x32x16_bf16 v[98:113], v[246:249], v[158:161], v[98:113]
	ds_read_b128 v[246:249], v243 offset:32768
	s_waitcnt lgkmcnt(3)
	v_mfma_f32_32x32x16_bf16 v[114:129], v[250:253], v[158:161], v[114:129]
	ds_read_b128 v[250:253], v243 offset:40960
	v_xor_b32_e32 v242, 0x80, v210
	v_xor_b32_e32 v243, 0x80, v211
	v_xor_b32_e32 v244, 0x80, v212
	v_xor_b32_e32 v245, 0x80, v213
	s_waitcnt lgkmcnt(3)
	v_mfma_f32_32x32x16_bf16 v[98:113], v[82:85], v[142:145], v[98:113]
	ds_read_b128 v[82:85], v244 offset:32768
	s_waitcnt lgkmcnt(3)
	v_mfma_f32_32x32x16_bf16 v[114:129], v[86:89], v[142:145], v[114:129]
	ds_read_b128 v[86:89], v244 offset:40960
	s_waitcnt lgkmcnt(3)
	v_mfma_f32_32x32x16_bf16 v[98:113], v[246:249], v[138:141], v[98:113]
	ds_read_b128 v[246:249], v245 offset:32768
	s_waitcnt lgkmcnt(3)
	v_mfma_f32_32x32x16_bf16 v[114:129], v[250:253], v[138:141], v[114:129]
	ds_read_b128 v[250:253], v245 offset:40960
	s_waitcnt lgkmcnt(3)
	v_mfma_f32_32x32x16_bf16 v[98:113], v[82:85], v[134:137], v[98:113]
	s_waitcnt lgkmcnt(2)
	v_mfma_f32_32x32x16_bf16 v[114:129], v[86:89], v[134:137], v[114:129]
	s_waitcnt lgkmcnt(1)
; __device__ __forceinline__ void finishSM(f32x16& p0, f32x16& p1, float alpha, float& l_reg, bf16x8& pa0, bf16x8& pa1, bf16x8& pa2, bf16x8& pa3) {
;     for (int r = 0; r < 16; ++r) p1[r] = __builtin_amdgcn_exp2f(p1[r]);
;     float ps = 0; for (int r = 0; r < 16; ++r) ps += p0[r]; for (int r = 0; r < 16; ++r) ps += p1[r];
;     { auto rr = __builtin_amdgcn_permlane32_swap(__float_as_uint(ps), __float_as_uint(ps), false, false);
;       ps = __uint_as_float(rr[0]) + __uint_as_float(rr[1]); }
;     l_reg = l_reg * alpha + ps;
;     ...
;     PK4(p0, 0, pa0); PK4(p0, 8, pa1); PK4(p1, 0, pa2); PK4(p1, 8, pa3);
;     ...
; }
; template <int KB, bool EXT>
; __device__ __forceinline__ void qkt(f32x16& p0, f32x16& p1, const char* lds, int r32, int hi, const bf16x8* qr, bf16x8 qx) {
;     p0 = f32x16{}; p1 = f32x16{};
;     const char* kb[4];
; #pragma unroll
;     for (int dd = 0; dd < 4; ++dd) kb[dd] = lds + OFF_K + KB * SHM_K + KSWZ(r32, (dd * 16 + hi * 8) * 2);
; #pragma unroll
;     for (int d0 = 0; d0 < 8; ++d0) { const char* a = kb[d0 & 3] + (d0 >> 2) * 128;
;         bf16x8 b0 = *reinterpret_cast<const bf16x8*>(a);
;         bf16x8 b1 = *reinterpret_cast<const bf16x8*>(a + 32 * 256);
;         p0 = __builtin_amdgcn_mfma_f32_32x32x16_bf16(b0, qr[d0], p0, 0, 0, 0);
;         p1 = __builtin_amdgcn_mfma_f32_32x32x16_bf16(b1, qr[d0], p1, 0, 0, 0); }
;     if (EXT) { const char* xa = lds + OFF_X + KB * SHM_X + r32 * 32 + hi * 16;
;         bf16x8 x0 = *reinterpret_cast<const bf16x8*>(xa), x1 = *reinterpret_cast<const bf16x8*>(xa + 32 * 32);
;         p0 = __builtin_amdgcn_mfma_f32_32x32x16_bf16(x0, qx, p0, 0, 0, 0);
;         p1 = __builtin_amdgcn_mfma_f32_32x32x16_bf16(x1, qx, p1, 0, 0, 0); }
; }
; template <int VB>
; __device__ __forceinline__ void pv_tile(f32x16* o, int vb0, bf16x8 pa0, bf16x8 pa1, bf16x8 pa2, bf16x8 pa3) {
;     ...
;     PV_D0(0); PV_D0(1); PV_D0(2); PV_D0(3);
	v_mfma_f32_32x32x16_bf16 v[98:113], v[246:249], v[130:133], v[98:113]
	v_exp_f32_e32 v82, v162
	v_add_f32_e32 v162, 0, v66
	v_add_f32_e32 v162, v67, v162
	v_add_f32_e32 v162, v68, v162
	v_add_f32_e32 v162, v69, v162
	v_add_f32_e32 v162, v70, v162
	v_add_f32_e32 v162, v71, v162
	v_add_f32_e32 v162, v72, v162
	v_add_f32_e32 v162, v73, v162
	v_add_f32_e32 v162, v74, v162
	v_add_f32_e32 v162, v75, v162
	v_add_f32_e32 v162, v76, v162
	v_add_f32_e32 v162, v77, v162
	v_add_f32_e32 v162, v78, v162
	v_exp_f32_e32 v83, v163
	v_add_f32_e32 v162, v79, v162
	v_exp_f32_e32 v84, v164
	v_add_f32_e32 v162, v80, v162
	v_exp_f32_e32 v85, v165
	v_add_f32_e32 v162, v81, v162
	s_waitcnt lgkmcnt(0)
	v_mfma_f32_32x32x16_bf16 v[114:129], v[250:253], v[130:133], v[114:129]
	v_exp_f32_e32 v86, v166
	v_add_f32_e32 v162, v82, v162
	v_exp_f32_e32 v87, v167
	v_add_f32_e32 v162, v83, v162
	v_exp_f32_e32 v88, v168
	v_add_f32_e32 v162, v84, v162
	v_exp_f32_e32 v89, v169
	v_add_f32_e32 v162, v85, v162
	v_add_f32_e32 v162, v86, v162
	v_add_f32_e32 v162, v87, v162
	v_add_f32_e32 v162, v88, v162
	v_add_f32_e32 v162, v89, v162
	v_add_f32_e32 v162, v90, v162
	v_add_f32_e32 v162, v91, v162
	v_add_f32_e32 v162, v92, v162
	v_add_f32_e32 v162, v93, v162
	v_add_f32_e32 v162, v94, v162
	v_add_f32_e32 v162, v95, v162
	v_add_f32_e32 v162, v96, v162
	v_add_f32_e32 v217, v97, v162
	v_mov_b32_e32 v218, v217
	v_cvt_pk_bf16_f32 v162, v66, v67
	v_cvt_pk_bf16_f32 v163, v68, v69
	v_cvt_pk_bf16_f32 v164, v70, v71
	v_cvt_pk_bf16_f32 v165, v72, v73
	v_cvt_pk_bf16_f32 v166, v74, v75
	v_cvt_pk_bf16_f32 v167, v76, v77
	v_cvt_pk_bf16_f32 v168, v78, v79
	v_cvt_pk_bf16_f32 v169, v80, v81
	v_cvt_pk_bf16_f32 v170, v82, v83
	v_cvt_pk_bf16_f32 v171, v84, v85
	v_cvt_pk_bf16_f32 v172, v86, v87
	v_cvt_pk_bf16_f32 v173, v88, v89
	v_cvt_pk_bf16_f32 v174, v90, v91
	v_cvt_pk_bf16_f32 v175, v92, v93
	v_cvt_pk_bf16_f32 v176, v94, v95
	v_cvt_pk_bf16_f32 v177, v96, v97
	s_nop 1
	v_permlane32_swap_b32_e32 v217, v218
	v_permlane32_swap_b32_e32 v162, v164
	v_permlane32_swap_b32_e32 v163, v165
	v_permlane32_swap_b32_e32 v166, v168
	v_permlane32_swap_b32_e32 v167, v169
	v_permlane32_swap_b32_e32 v170, v172
	v_permlane32_swap_b32_e32 v171, v173
	v_permlane32_swap_b32_e32 v174, v176
	v_permlane32_swap_b32_e32 v175, v177
	ds_read_b64_tr_b16 v[222:223], v194 offset:0x4000
	ds_read_b64_tr_b16 v[224:225], v194 offset:0x4800
	ds_read_b64_tr_b16 v[226:227], v194 offset:0x5000
	ds_read_b64_tr_b16 v[228:229], v194 offset:0x5800
	ds_read_b64_tr_b16 v[230:231], v194 offset:0x6000
	ds_read_b64_tr_b16 v[232:233], v194 offset:0x6800
	ds_read_b64_tr_b16 v[234:235], v194 offset:0x7000
	ds_read_b64_tr_b16 v[236:237], v194 offset:0x7800
	s_waitcnt lgkmcnt(0)
	s_nop 0
	v_mfma_f32_32x32x16_bf16 v[2:17], v[162:165], v[222:225], v[2:17]
	ds_read_b64_tr_b16 v[222:223], v194 offset:0x4200
	ds_read_b64_tr_b16 v[224:225], v194 offset:0x4a00
	v_mfma_f32_32x32x16_bf16 v[2:17], v[166:169], v[226:229], v[2:17]
	ds_read_b64_tr_b16 v[226:227], v194 offset:0x5200
	ds_read_b64_tr_b16 v[228:229], v194 offset:0x5a00
	v_mfma_f32_32x32x16_bf16 v[2:17], v[170:173], v[230:233], v[2:17]
	ds_read_b64_tr_b16 v[230:231], v194 offset:0x6200
	ds_read_b64_tr_b16 v[232:233], v194 offset:0x6a00
	v_mfma_f32_32x32x16_bf16 v[2:17], v[174:177], v[234:237], v[2:17]
	ds_read_b64_tr_b16 v[234:235], v194 offset:0x7200
	ds_read_b64_tr_b16 v[236:237], v194 offset:0x7a00
	s_waitcnt lgkmcnt(0)
	v_mfma_f32_32x32x16_bf16 v[50:65], v[162:165], v[222:225], v[50:65]
	ds_read_b64_tr_b16 v[222:223], v194 offset:0x4400
	ds_read_b64_tr_b16 v[224:225], v194 offset:0x4c00
	v_mfma_f32_32x32x16_bf16 v[50:65], v[166:169], v[226:229], v[50:65]
	ds_read_b64_tr_b16 v[226:227], v194 offset:0x5400
	ds_read_b64_tr_b16 v[228:229], v194 offset:0x5c00
	v_mfma_f32_32x32x16_bf16 v[50:65], v[170:173], v[230:233], v[50:65]
	ds_read_b64_tr_b16 v[230:231], v194 offset:0x6400
	ds_read_b64_tr_b16 v[232:233], v194 offset:0x6c00
	v_mfma_f32_32x32x16_bf16 v[50:65], v[174:177], v[234:237], v[50:65]
	ds_read_b64_tr_b16 v[234:235], v194 offset:0x7400
	ds_read_b64_tr_b16 v[236:237], v194 offset:0x7c00
	s_waitcnt lgkmcnt(0)
	v_mfma_f32_32x32x16_bf16 v[34:49], v[162:165], v[222:225], v[34:49]
	ds_read_b64_tr_b16 v[222:223], v194 offset:0x4600
	ds_read_b64_tr_b16 v[224:225], v194 offset:0x4e00
	v_mfma_f32_32x32x16_bf16 v[34:49], v[166:169], v[226:229], v[34:49]
	ds_read_b64_tr_b16 v[226:227], v194 offset:0x5600
	ds_read_b64_tr_b16 v[228:229], v194 offset:0x5e00
	v_mfma_f32_32x32x16_bf16 v[34:49], v[170:173], v[230:233], v[34:49]
	ds_read_b64_tr_b16 v[230:231], v194 offset:0x6600
	ds_read_b64_tr_b16 v[232:233], v194 offset:0x6e00
	v_mfma_f32_32x32x16_bf16 v[34:49], v[174:177], v[234:237], v[34:49]
	ds_read_b64_tr_b16 v[234:235], v194 offset:0x7600
	ds_read_b64_tr_b16 v[236:237], v194 offset:0x7e00
	s_waitcnt lgkmcnt(0)
	s_waitcnt vmcnt(0)
	s_cmp_eq_u32 s99, 0
	s_cbranch_scc1 .Lstg_p1b
	s_barrier

; template <int MODE> ...
;     ...
;         const int tdiag = P0 / KVBLK; int r = 1;
;         for (; r + 1 < NTr && jb + r + 1 <= tdiag; r += 2) {
;             HALFU(pB0, pB1, mnB, alB, pA0, pA1, alA, jb + r, 1, 0);
;             HALFU(pA0, pA1, mnA, alA, pB0, pB1, alB, jb + r + 1, 0, 1);
;         }
;         for (; r + 1 < NTr; r += 2) {
;             HALF(pB0, pB1, mnB, alB, pA0, pA1, alA, jb + r, 1, 0);
;             HALF(pA0, pA1, mnA, alA, pB0, pB1, alB, jb + r + 1, 0, 1);
;         }
.LBB0_1184:
	s_add_i32 s71, s60, 1
	s_cmp_lg_u32 0, -1
	s_cselect_b32 s0, 0, 0
	s_add_i32 s0, s0, s72
	s_add_i32 s27, s0, 0x6000
	s_add_i32 s0, s61, s26
	s_lshl_b32 s6, s0, 6
	s_add_i32 s4, s6, 0x80
	s_mov_b32 s5, s11
	s_lshl_b64 s[4:5], s[4:5], 8
	s_add_u32 s72, s18, s4
	s_mov_b32 s1, s11
	s_addc_u32 s73, s19, s5
	s_lshl_b64 s[4:5], s[0:1], 14
	s_add_u32 s74, s20, s4
	s_addc_u32 s75, s21, s5
	s_add_i32 s4, s6, 64
	s_mov_b32 s5, s11
	s_lshl_b64 s[4:5], s[4:5], 8
	s_add_u32 s76, s20, s4
	s_addc_u32 s77, s21, s5
	s_add_u32 s78, s18, s4
	s_addc_u32 s79, s19, s5
	s_lshl_b64 s[0:1], s[0:1], 3
	v_and_b32_e32 v182, 0xf0, v199
	s_add_u32 s0, s47, s0
	v_xad_u32 v184, v182, v207, 0
	v_xad_u32 v185, v203, v182, 0
	v_xad_u32 v211, v201, v182, 0
	v_xad_u32 v212, v200, v182, 0
	s_addc_u32 s1, s48, s1
	v_lshl_add_u32 v208, v190, 2, s62
	v_add_u32_e32 v207, s62, v207
	v_lshl_add_u64 v[182:183], s[0:1], 0, v[178:179]
	s_mov_b64 s[0:1], 0
	v_add_u32_e32 v209, v184, v198
	v_add_u32_e32 v210, v185, v198
	v_add_u32_e32 v211, v211, v198
	v_add_u32_e32 v212, v212, v198
	s_branch .LBB0_1188

; template <int KB, bool EXT>
; __device__ __forceinline__ void qkt(f32x16& p0, f32x16& p1, const char* lds, int r32, int hi, const bf16x8* qr, bf16x8 qx) {
;     ...
;     for (int dd = 0; dd < 4; ++dd) kb[dd] = lds + OFF_K + KB * SHM_K + KSWZ(r32, (dd * 16 + hi * 8) * 2);
; #pragma unroll
;     for (int d0 = 0; d0 < 8; ++d0) { const char* a = kb[d0 & 3] + (d0 >> 2) * 128;
;         bf16x8 b0 = *reinterpret_cast<const bf16x8*>(a);
;         bf16x8 b1 = *reinterpret_cast<const bf16x8*>(a + 32 * 256);
;         p0 = __builtin_amdgcn_mfma_f32_32x32x16_bf16(b0, qr[d0], p0, 0, 0, 0);
;         p1 = __builtin_amdgcn_mfma_f32_32x32x16_bf16(b1, qr[d0], p1, 0, 0, 0); }
.LBB0_1188:
	global_load_dwordx2 v[184:185], v[182:183], off offset:-8
	s_add_i32 s80, s61, s26
	s_add_u32 s4, s78, s0
	s_addc_u32 s5, s79, s1
	s_mov_b32 s6, m0
	s_mov_b32 m0, s64
	s_nop 0
	global_load_lds_dwordx4 v204, s[4:5]
	s_mov_b32 m0, s6
	s_nop 0
	s_mov_b32 s6, m0
	s_mov_b32 m0, s65
	s_nop 0
	global_load_lds_dwordx4 v205, s[4:5]
	s_mov_b32 m0, s6
	s_add_u32 s4, s74, s0
	s_addc_u32 s5, s75, s1
	s_mov_b32 s6, m0
	s_mov_b32 m0, s33
	s_nop 0
	global_load_lds_dwordx4 v196, s[4:5]
	s_mov_b32 m0, s6
	s_nop 0
	s_mov_b32 s6, m0
	s_mov_b32 m0, s27
	s_nop 0
	global_load_lds_dwordx4 v197, s[4:5]
	s_mov_b32 m0, s6
	s_cmp_le_u32 s80, s60
	s_cselect_b64 s[6:7], -1, 0
	s_cmp_gt_u32 s80, s60
	s_cbranch_scc1 .LBB0_1190
	ds_read_b128 v[66:69], v209 offset:49152
	ds_read_b128 v[82:85], v209 offset:57344
	ds_read_b128 v[214:217], v210 offset:49152
	s_waitcnt lgkmcnt(2)
	v_mfma_f32_32x32x16_bf16 v[66:81], v[66:69], v[146:149], 0
	s_waitcnt lgkmcnt(0)
	v_mfma_f32_32x32x16_bf16 v[66:81], v[214:217], v[150:153], v[66:81]
	ds_read_b128 v[214:217], v210 offset:57344
	v_mfma_f32_32x32x16_bf16 v[82:97], v[82:85], v[146:149], 0
	s_waitcnt lgkmcnt(0)
	v_mfma_f32_32x32x16_bf16 v[82:97], v[214:217], v[150:153], v[82:97]
	ds_read_b128 v[214:217], v211 offset:49152
	s_waitcnt lgkmcnt(0)
	v_mfma_f32_32x32x16_bf16 v[66:81], v[214:217], v[154:157], v[66:81]
	ds_read_b128 v[214:217], v211 offset:57344
	s_waitcnt lgkmcnt(0)
	v_mfma_f32_32x32x16_bf16 v[82:97], v[214:217], v[154:157], v[82:97]
	ds_read_b128 v[214:217], v212 offset:49152
	s_waitcnt lgkmcnt(0)
	v_mfma_f32_32x32x16_bf16 v[66:81], v[214:217], v[158:161], v[66:81]
	ds_read_b128 v[214:217], v212 offset:57344
	s_waitcnt lgkmcnt(0)
	v_mfma_f32_32x32x16_bf16 v[82:97], v[214:217], v[158:161], v[82:97]
	v_xor_b32_e32 v242, 0x80, v209
	v_xor_b32_e32 v243, 0x80, v210
	v_xor_b32_e32 v244, 0x80, v211
	v_xor_b32_e32 v245, 0x80, v212
	ds_read_b128 v[214:217], v242 offset:49152
	s_waitcnt lgkmcnt(0)
	v_mfma_f32_32x32x16_bf16 v[66:81], v[214:217], v[142:145], v[66:81]
	ds_read_b128 v[214:217], v242 offset:57344
	s_waitcnt lgkmcnt(0)
	v_mfma_f32_32x32x16_bf16 v[82:97], v[214:217], v[142:145], v[82:97]
	ds_read_b128 v[214:217], v243 offset:49152
	s_waitcnt lgkmcnt(0)
	v_mfma_f32_32x32x16_bf16 v[66:81], v[214:217], v[138:141], v[66:81]
	ds_read_b128 v[214:217], v243 offset:57344
	s_waitcnt lgkmcnt(0)
	v_mfma_f32_32x32x16_bf16 v[82:97], v[214:217], v[138:141], v[82:97]
	ds_read_b128 v[214:217], v244 offset:49152
	s_waitcnt lgkmcnt(0)
	v_mfma_f32_32x32x16_bf16 v[66:81], v[214:217], v[134:137], v[66:81]
	ds_read_b128 v[214:217], v244 offset:57344
	s_waitcnt lgkmcnt(0)
	v_mfma_f32_32x32x16_bf16 v[82:97], v[214:217], v[134:137], v[82:97]
	ds_read_b128 v[214:217], v245 offset:49152
	s_waitcnt lgkmcnt(0)
	v_mfma_f32_32x32x16_bf16 v[66:81], v[214:217], v[130:133], v[66:81]
	ds_read_b128 v[214:217], v245 offset:57344
	s_waitcnt lgkmcnt(0)
	v_mfma_f32_32x32x16_bf16 v[82:97], v[214:217], v[130:133], v[82:97]

; template <int KB, bool EXT>
; __device__ __forceinline__ void qkt(f32x16& p0, f32x16& p1, const char* lds, int r32, int hi, const bf16x8* qr, bf16x8 qx) {
;     ...
;     for (int dd = 0; dd < 4; ++dd) kb[dd] = lds + OFF_K + KB * SHM_K + KSWZ(r32, (dd * 16 + hi * 8) * 2);
; #pragma unroll
;     for (int d0 = 0; d0 < 8; ++d0) { const char* a = kb[d0 & 3] + (d0 >> 2) * 128;
;         bf16x8 b0 = *reinterpret_cast<const bf16x8*>(a);
;         bf16x8 b1 = *reinterpret_cast<const bf16x8*>(a + 32 * 256);
;         p0 = __builtin_amdgcn_mfma_f32_32x32x16_bf16(b0, qr[d0], p0, 0, 0, 0);
;         p1 = __builtin_amdgcn_mfma_f32_32x32x16_bf16(b1, qr[d0], p1, 0, 0, 0); }
.LBB0_1202:
	s_add_u32 s6, s76, s0
	s_addc_u32 s7, s77, s1
	s_mov_b32 s24, m0
	s_mov_b32 m0, s63
	s_nop 0
	global_load_lds_dwordx4 v196, s[6:7]
	s_mov_b32 m0, s24
	s_nop 0
	s_mov_b32 s24, m0
	s_mov_b32 m0, s68
	s_nop 0
	global_load_lds_dwordx4 v197, s[6:7]
	s_mov_b32 m0, s24
	s_cmp_lt_u32 s80, s60
	s_cselect_b64 s[6:7], -1, 0
	s_cmp_ge_u32 s80, s60
	s_cbranch_scc1 .LBB0_1204
	ds_read_b128 v[98:101], v209 offset:32768
	ds_read_b128 v[114:117], v209 offset:40960
	ds_read_b128 v[214:217], v210 offset:32768
	s_waitcnt lgkmcnt(2)
	v_mfma_f32_32x32x16_bf16 v[98:113], v[98:101], v[146:149], 0
	s_waitcnt lgkmcnt(0)
	v_mfma_f32_32x32x16_bf16 v[98:113], v[214:217], v[150:153], v[98:113]
	ds_read_b128 v[214:217], v210 offset:40960
	v_mfma_f32_32x32x16_bf16 v[114:129], v[114:117], v[146:149], 0
	s_waitcnt lgkmcnt(0)
	v_mfma_f32_32x32x16_bf16 v[114:129], v[214:217], v[150:153], v[114:129]
	ds_read_b128 v[214:217], v211 offset:32768
	s_waitcnt lgkmcnt(0)
	v_mfma_f32_32x32x16_bf16 v[98:113], v[214:217], v[154:157], v[98:113]
	ds_read_b128 v[214:217], v211 offset:40960
	s_waitcnt lgkmcnt(0)
	v_mfma_f32_32x32x16_bf16 v[114:129], v[214:217], v[154:157], v[114:129]
	ds_read_b128 v[214:217], v212 offset:32768
	s_waitcnt lgkmcnt(0)
	v_mfma_f32_32x32x16_bf16 v[98:113], v[214:217], v[158:161], v[98:113]
	ds_read_b128 v[214:217], v212 offset:40960
	s_waitcnt lgkmcnt(0)
	v_mfma_f32_32x32x16_bf16 v[114:129], v[214:217], v[158:161], v[114:129]
	v_xor_b32_e32 v242, 0x80, v209
	v_xor_b32_e32 v243, 0x80, v210
	v_xor_b32_e32 v244, 0x80, v211
	v_xor_b32_e32 v245, 0x80, v212
	ds_read_b128 v[214:217], v242 offset:32768
	s_waitcnt lgkmcnt(0)
	v_mfma_f32_32x32x16_bf16 v[98:113], v[214:217], v[142:145], v[98:113]
	ds_read_b128 v[214:217], v242 offset:40960
	s_waitcnt lgkmcnt(0)
	v_mfma_f32_32x32x16_bf16 v[114:129], v[214:217], v[142:145], v[114:129]
	ds_read_b128 v[214:217], v243 offset:32768
	s_waitcnt lgkmcnt(0)
	v_mfma_f32_32x32x16_bf16 v[98:113], v[214:217], v[138:141], v[98:113]
	ds_read_b128 v[214:217], v243 offset:40960
	s_waitcnt lgkmcnt(0)
	v_mfma_f32_32x32x16_bf16 v[114:129], v[214:217], v[138:141], v[114:129]
	ds_read_b128 v[214:217], v244 offset:32768
	s_waitcnt lgkmcnt(0)
	v_mfma_f32_32x32x16_bf16 v[98:113], v[214:217], v[134:137], v[98:113]
	ds_read_b128 v[214:217], v244 offset:40960
	s_waitcnt lgkmcnt(0)
	v_mfma_f32_32x32x16_bf16 v[114:129], v[214:217], v[134:137], v[114:129]
	ds_read_b128 v[214:217], v245 offset:32768
	s_waitcnt lgkmcnt(0)
	v_mfma_f32_32x32x16_bf16 v[98:113], v[214:217], v[130:133], v[98:113]
	ds_read_b128 v[214:217], v245 offset:40960
	s_waitcnt lgkmcnt(0)
	v_mfma_f32_32x32x16_bf16 v[114:129], v[214:217], v[130:133], v[114:129]

; #define SBAR() __builtin_amdgcn_sched_barrier(0)
; template <int KB, bool EXT>
; __device__ __forceinline__ void qkt(f32x16& p0, f32x16& p1, const char* lds, int r32, int hi, const bf16x8* qr, bf16x8 qx) {
;     ...
;     for (int dd = 0; dd < 4; ++dd) kb[dd] = lds + OFF_K + KB * SHM_K + KSWZ(r32, (dd * 16 + hi * 8) * 2);
; #pragma unroll
;     for (int d0 = 0; d0 < 8; ++d0) { const char* a = kb[d0 & 3] + (d0 >> 2) * 128;
;         bf16x8 b0 = *reinterpret_cast<const bf16x8*>(a);
;         bf16x8 b1 = *reinterpret_cast<const bf16x8*>(a + 32 * 256);
;         p0 = __builtin_amdgcn_mfma_f32_32x32x16_bf16(b0, qr[d0], p0, 0, 0, 0);
;         p1 = __builtin_amdgcn_mfma_f32_32x32x16_bf16(b1, qr[d0], p1, 0, 0, 0); }
; template <int MODE> ...
;     ...
;         HALF(pB0, pB1, mnB, alB, pA0, pA1, alA, je - 1, 1, 0);
;         if (ACT(je - 1)) { finishSM(pB0, pB1, alB, l_reg, pa0, pa1, pa2, pa3); SBAR(); pv_tile<1>(o, vb0, pa0, pa1, pa2, pa3); }
.LBB0_1213:
	s_add_i32 s2, s69, -1
	s_mov_b32 s3, s11
	s_lshl_b64 s[0:1], s[2:3], 3
	s_add_u32 s0, s37, s0
	s_addc_u32 s1, s38, s1
	v_lshl_add_u64 v[182:183], s[0:1], 0, v[178:179]
	global_load_dwordx2 v[182:183], v[182:183], off
	s_lshl_b32 s0, s2, 6
	s_mov_b32 s1, s11
	s_lshl_b64 s[0:1], s[0:1], 8
	s_add_u32 s0, s20, s0
	s_addc_u32 s1, s21, s1
	s_mov_b32 s3, m0
	s_mov_b32 m0, s33
	s_nop 0
	global_load_lds_dwordx4 v196, s[0:1]
	s_mov_b32 m0, s3
	s_nop 0
	s_mov_b32 s3, m0
	s_mov_b32 m0, s27
	s_nop 0
	global_load_lds_dwordx4 v197, s[0:1]
	s_mov_b32 m0, s3
	s_cmp_le_i32 s2, s60
	s_cselect_b64 s[0:1], -1, 0
	s_cmp_gt_i32 s2, s60
	s_cbranch_scc1 .LBB0_1215
	v_bitop3_b32 v66, v203, v199, s50 bitop3:0x78
	s_waitcnt vmcnt(1)
	v_add3_u32 v184, 0, v66, v198
	v_bitop3_b32 v66, v201, v199, s50 bitop3:0x78
	v_add3_u32 v178, 0, v202, v198
	v_add3_u32 v185, 0, v66, v198
	v_bitop3_b32 v66, v200, v199, s50 bitop3:0x78
	v_add3_u32 v200, 0, v66, v198
	ds_read_b128 v[66:69], v178 offset:49152
	ds_read_b128 v[82:85], v178 offset:57344
	s_waitcnt lgkmcnt(1)
	v_mfma_f32_32x32x16_bf16 v[66:81], v[66:69], v[146:149], 0
	s_waitcnt lgkmcnt(0)
	v_mfma_f32_32x32x16_bf16 v[82:97], v[82:85], v[146:149], 0
	ds_read_b128 v[146:149], v184 offset:49152
	ds_read_b128 v[196:199], v184 offset:57344
	s_waitcnt lgkmcnt(1)
	v_mfma_f32_32x32x16_bf16 v[66:81], v[146:149], v[150:153], v[66:81]
	s_waitcnt lgkmcnt(0)
	v_mfma_f32_32x32x16_bf16 v[82:97], v[196:199], v[150:153], v[82:97]
	ds_read_b128 v[146:149], v185 offset:49152
	ds_read_b128 v[150:153], v185 offset:57344
	s_waitcnt lgkmcnt(1)
	v_mfma_f32_32x32x16_bf16 v[66:81], v[146:149], v[154:157], v[66:81]
	s_waitcnt lgkmcnt(0)
	v_mfma_f32_32x32x16_bf16 v[82:97], v[150:153], v[154:157], v[82:97]
	ds_read_b128 v[146:149], v200 offset:49152
	ds_read_b128 v[150:153], v200 offset:57344
	s_waitcnt lgkmcnt(1)
	v_mfma_f32_32x32x16_bf16 v[66:81], v[146:149], v[158:161], v[66:81]
	s_waitcnt lgkmcnt(0)
	v_mfma_f32_32x32x16_bf16 v[82:97], v[150:153], v[158:161], v[82:97]
	v_xor_b32_e32 v242, 0x80, v178
	v_xor_b32_e32 v243, 0x80, v184
	v_xor_b32_e32 v244, 0x80, v185
	v_xor_b32_e32 v245, 0x80, v200
	ds_read_b128 v[146:149], v242 offset:49152
	ds_read_b128 v[150:153], v242 offset:57344
	s_waitcnt lgkmcnt(1)
	v_mfma_f32_32x32x16_bf16 v[66:81], v[146:149], v[142:145], v[66:81]
	s_waitcnt lgkmcnt(0)
	v_mfma_f32_32x32x16_bf16 v[82:97], v[150:153], v[142:145], v[82:97]
	ds_read_b128 v[142:145], v243 offset:49152
	ds_read_b128 v[146:149], v243 offset:57344
	s_waitcnt lgkmcnt(1)
	v_mfma_f32_32x32x16_bf16 v[66:81], v[142:145], v[138:141], v[66:81]
	s_waitcnt lgkmcnt(0)
	v_mfma_f32_32x32x16_bf16 v[82:97], v[146:149], v[138:141], v[82:97]
	ds_read_b128 v[138:141], v244 offset:49152
	ds_read_b128 v[142:145], v244 offset:57344
	s_waitcnt lgkmcnt(1)
	v_mfma_f32_32x32x16_bf16 v[66:81], v[138:141], v[134:137], v[66:81]
	s_waitcnt lgkmcnt(0)
	v_mfma_f32_32x32x16_bf16 v[82:97], v[142:145], v[134:137], v[82:97]
	ds_read_b128 v[134:137], v245 offset:49152
	ds_read_b128 v[138:141], v245 offset:57344
	s_waitcnt lgkmcnt(1)
	v_mfma_f32_32x32x16_bf16 v[66:81], v[134:137], v[130:133], v[66:81]
	s_waitcnt lgkmcnt(0)
	v_mfma_f32_32x32x16_bf16 v[82:97], v[138:141], v[130:133], v[82:97]

; #define VM_WAIT() asm volatile("s_waitcnt vmcnt(0)" ::: "memory")
; #define KDMA(k0, bf) do { const bf16_t* kb_ = Kh + (size_t)(k0) * D; _Pragma("unroll") for (int i_ = 0; i_ < 2; ++i_) pg8::glds16_s((const void*)kb_, koff[i_], ldsb + OFF_K + (bf) * SHM_K + wid * 1024 + i_ * 8192); } while (0)
; #define VDMA(k0, bf) do { const bf16_t* vb_ = Vh + (size_t)(k0) * D; _Pragma("unroll") for (int i_ = 0; i_ < 2; ++i_) pg8::glds16_s((const void*)vb_, voff[i_], ldsb + OFF_V + (bf) * SHM_V + wid * 1024 + i_ * 8192); } while (0)
; #define XLOAD(k0) do { if (tid < 128 && xhalf == 0) st_x = *reinterpret_cast<const bf16x8*>((const char*)(KXh + (size_t)(k0) * 8) + xo); } while (0)
; #define XWRITE(bf) do { if (tid < 128) *(bf16x8*)(lds + OFF_X + (bf) * SHM_X + xkey * 32 + xhalf * 16) = st_x; } while (0)
; template <int MODE> ...
;     ...
;     unsigned koff[2], voff[2];
; #pragma unroll
;     for (int i = 0; i < 2; ++i) { const int q = tid * 16 + i * 8192;
;         { const int row = q >> 8, colB = (q & 255) ^ ((row & 7) << 4); koff[i] = (unsigned)(row * 256 + colB); }
;         { const int sb = q >> 9, w = q & 511, kk = (sb >> 2) * 8 + (w >> 6), k = (kk & ~0xC) | ((kk & 4) << 1) | ((kk & 8) >> 1), col = (sb & 3) * 32 + ((w & 63) >> 4) * 8; voff[i] = (unsigned)(k * 256 + col * 2); } }
;     ...
;         bf16x8 st_x = (bf16x8){0, 0, 0, 0, 0, 0, 0, 0};
;         const int xkey = tid >> 1, xhalf = tid & 1; const unsigned xo = (unsigned)xkey * 16u;
;     ...
;         KDMA(jb * KVBLK, 0); VDMA(jb * KVBLK, 0); XLOAD(jb * KVBLK); VM_WAIT(); XWRITE(0); __syncthreads();
.LBB0_1374:
	s_or_b64 exec, exec, s[0:1]
	s_and_b32 s12, s3, 0xffffffc0
	v_add_u32_e32 v9, s12, v83
	v_lshlrev_b32_e32 v5, 3, v83
	v_lshlrev_b32_e32 v4, 4, v9
	v_and_b32_e32 v7, 0xf0, v9
	s_movk_i32 s0, 0xf0
	v_and_b32_e32 v6, 24, v5
	v_bitop3_b32 v7, v4, v7, s0 bitop3:0x6c
	v_bfe_u32 v8, v9, 2, 2
	v_lshrrev_b32_e32 v10, 1, v9
	s_movk_i32 s0, 0x60
	v_and_or_b32 v8, v10, 8, v8
	v_and_or_b32 v10, v9, s0, v6
	s_movk_i32 s0, 0xff00
	s_lshl_b32 s74, s76, 6
	v_and_or_b32 v164, v4, s0, v7
	v_add_u32_e32 v4, 0x2000, v4
	s_ashr_i32 s75, s74, 31
	v_and_or_b32 v166, v4, s0, v7
	s_lshl_b64 s[0:1], s[74:75], 8
	v_readlane_b32 s3, v240, 56
	s_add_u32 s6, s3, s0
	s_addc_u32 s7, s86, s1
	s_lshl_b32 s11, s2, 10
	s_cmp_lg_u32 0, -1
	s_cselect_b32 s2, 0, 0
	s_add_i32 s92, s11, s2
	v_ashrrev_i32_e32 v11, 4, v9
	s_barrier
	s_add_i32 s93, s92, 0x8000
	s_mov_b32 s2, m0
	s_mov_b32 m0, s93
	s_nop 0
	global_load_lds_dwordx4 v164, s[6:7]
	s_mov_b32 m0, s2
	v_and_b32_e32 v12, 0xfffff0, v11
	v_lshrrev_b32_e32 v11, 1, v11
	v_ashrrev_i32_e32 v4, 8, v4
	s_add_i32 s96, s92, 0xa000
	s_mov_b32 s2, m0
	s_mov_b32 m0, s96
	s_nop 0
	global_load_lds_dwordx4 v166, s[6:7]
	s_mov_b32 m0, s2
	v_and_b32_e32 v11, 4, v11
	v_and_b32_e32 v7, 0xfffff0, v4
	v_lshrrev_b32_e32 v4, 1, v4
	v_readlane_b32 s2, v240, 4
	v_lshlrev_b32_e32 v10, 1, v10
	v_or3_b32 v11, v12, v11, v8
	v_and_b32_e32 v4, 4, v4
	s_add_u32 s0, s2, s0
	v_lshl_or_b32 v165, v11, 8, v10
	v_or3_b32 v4, v7, v4, v8
	s_addc_u32 s1, s33, s1
	s_mov_b32 s2, m0
	s_mov_b32 m0, s92
	s_nop 0
	global_load_lds_dwordx4 v165, s[0:1]
	s_mov_b32 m0, s2
	v_lshl_or_b32 v167, v4, 8, v10
	v_and_b32_e32 v8, 1, v83
	s_add_i32 s97, s92, 0x2000
	s_mov_b32 s2, m0
	s_mov_b32 m0, s97
	s_nop 0
	global_load_lds_dwordx4 v167, s[0:1]
	s_mov_b32 m0, s2
	s_movk_i32 s0, 0x80
	v_ashrrev_i32_e32 v7, 1, v9
	v_cmp_gt_i32_e64 s[6:7], s0, v9
	v_cmp_eq_u32_e64 s[2:3], 0, v8
	v_lshlrev_b32_e32 v4, 4, v7
	s_and_b64 s[0:1], s[2:3], s[6:7]
	v_mov_b32_e32 v150, v3
	v_mov_b32_e32 v151, v3
	v_mov_b32_e32 v152, v3
	v_mov_b32_e32 v153, v3
	s_and_saveexec_b64 s[8:9], s[0:1]
	s_cbranch_execz .LBB0_1376
	s_lshl_b64 s[14:15], s[74:75], 4
	v_readlane_b32 s16, v240, 12
	v_readlane_b32 s17, v240, 13
	s_add_u32 s14, s16, s14
	s_addc_u32 s15, s17, s15
	global_load_dwordx4 v[150:153], v4, s[14:15]

; #define VM_WAIT() asm volatile("s_waitcnt vmcnt(0)" ::: "memory")
; #define KDMA(k0, bf) do { const bf16_t* kb_ = Kh + (size_t)(k0) * D; _Pragma("unroll") for (int i_ = 0; i_ < 2; ++i_) pg8::glds16_s((const void*)kb_, koff[i_], ldsb + OFF_K + (bf) * SHM_K + wid * 1024 + i_ * 8192); } while (0)
; #define VDMA(k0, bf) do { const bf16_t* vb_ = Vh + (size_t)(k0) * D; _Pragma("unroll") for (int i_ = 0; i_ < 2; ++i_) pg8::glds16_s((const void*)vb_, voff[i_], ldsb + OFF_V + (bf) * SHM_V + wid * 1024 + i_ * 8192); } while (0)
; #define XLOAD(k0) do { if (tid < 128 && xhalf == 0) st_x = *reinterpret_cast<const bf16x8*>((const char*)(KXh + (size_t)(k0) * 8) + xo); } while (0)
; #define XWRITE(bf) do { if (tid < 128) *(bf16x8*)(lds + OFF_X + (bf) * SHM_X + xkey * 32 + xhalf * 16) = st_x; } while (0)
; __device__ __forceinline__ void mask_causal(f32x16& p0, f32x16& p1, int dq) {
;     const float NEG = -__builtin_inff();
; #pragma unroll
;     for (int r = 0; r < 16; ++r) { const int c = (r & 3) + 8 * (r >> 2); if (dq - c < 0) p0[r] = NEG; if (dq - c - 32 < 0) p1[r] = NEG; }
; }
; template <int MODE> ...
;     ...
;         bf16x8 st_x = (bf16x8){0, 0, 0, 0, 0, 0, 0, 0};
;         const int xkey = tid >> 1, xhalf = tid & 1; const unsigned xo = (unsigned)xkey * 16u;
;     ...
;         KDMA(jb * KVBLK, 0); VDMA(jb * KVBLK, 0); XLOAD(jb * KVBLK); VM_WAIT(); XWRITE(0); __syncthreads();
;     ...
;         for (int t = jb; t < je; t += 2) { STEP(t, 0); STEP(t + 1, 1); }
.LBB0_1378:
	s_or_b64 exec, exec, s[8:9]
	s_lshl_b32 s8, s10, 2
	s_sub_i32 s87, 0x80, s8
	s_lshl_b32 s8, s12, 2
	s_add_i32 s8, s8, 0
	v_lshlrev_b32_e32 v162, 2, v82
	s_add_i32 s8, s8, 0x11000
	v_mov_b32_e32 v81, 0
	s_cmp_ge_i32 s76, s87
	v_lshl_add_u32 v163, v161, 2, s8
	v_lshl_add_u32 v160, v162, 2, s8
	v_mov_b32_e32 v80, 0
	v_mov_b32_e32 v79, 0
	v_mov_b32_e32 v78, 0
	v_mov_b32_e32 v77, 0
	v_mov_b32_e32 v76, 0
	v_mov_b32_e32 v75, 0
	v_mov_b32_e32 v74, 0
	v_mov_b32_e32 v73, 0
	v_mov_b32_e32 v72, 0
	v_mov_b32_e32 v71, 0
	v_mov_b32_e32 v70, 0
	v_mov_b32_e32 v69, 0
	v_mov_b32_e32 v68, 0
	v_mov_b32_e32 v67, 0
	v_mov_b32_e32 v66, 0
	v_mov_b32_e32 v65, 0
	v_mov_b32_e32 v64, 0
	v_mov_b32_e32 v63, 0
	v_mov_b32_e32 v62, 0
	v_mov_b32_e32 v61, 0
	v_mov_b32_e32 v60, 0
	v_mov_b32_e32 v59, 0
	v_mov_b32_e32 v58, 0
	v_mov_b32_e32 v57, 0
	v_mov_b32_e32 v56, 0
	v_mov_b32_e32 v55, 0
	v_mov_b32_e32 v54, 0
	v_mov_b32_e32 v53, 0
	v_mov_b32_e32 v52, 0
	v_mov_b32_e32 v51, 0
	v_mov_b32_e32 v50, 0
	v_mov_b32_e32 v49, 0
	v_mov_b32_e32 v48, 0
	v_mov_b32_e32 v47, 0
	v_mov_b32_e32 v46, 0
	v_mov_b32_e32 v45, 0
	v_mov_b32_e32 v44, 0
	v_mov_b32_e32 v43, 0
	v_mov_b32_e32 v42, 0
	v_mov_b32_e32 v41, 0
	v_mov_b32_e32 v40, 0
	v_mov_b32_e32 v39, 0
	v_mov_b32_e32 v38, 0
	v_mov_b32_e32 v37, 0
	v_mov_b32_e32 v36, 0
	v_mov_b32_e32 v35, 0
	v_mov_b32_e32 v34, 0
	v_mov_b32_e32 v33, 0
	v_mov_b32_e32 v32, 0
	v_mov_b32_e32 v31, 0
	v_mov_b32_e32 v30, 0
	v_mov_b32_e32 v29, 0
	v_mov_b32_e32 v28, 0
	v_mov_b32_e32 v27, 0
	v_mov_b32_e32 v26, 0
	v_mov_b32_e32 v25, 0
	v_mov_b32_e32 v24, 0
	v_mov_b32_e32 v23, 0
	v_mov_b32_e32 v22, 0
	v_mov_b32_e32 v21, 0
	v_mov_b32_e32 v20, 0
	v_mov_b32_e32 v19, 0
	v_mov_b32_e32 v18, 0
	v_mov_b32_e32 v178, 0
	s_waitcnt lgkmcnt(0)
	s_barrier
	s_cbranch_scc1 .LBB0_1410
	v_lshlrev_b32_e32 v9, 1, v83
	v_readlane_b32 s12, v240, 8
	v_lshlrev_b32_e32 v8, 4, v83
	v_and_b32_e32 v9, 32, v9
	s_movk_i32 s8, 0xc0
	s_lshr_b32 s88, s12, 6
	v_and_or_b32 v8, v8, s8, v9
	v_and_b32_e32 v5, 0x100, v5
	s_cmp_lg_u32 0, -1
	v_or3_b32 v5, v8, v5, v6
	s_cselect_b32 s8, 0, 0
	v_add_u32_e32 v168, s8, v5
	s_add_i32 s8, s8, s11
	v_readlane_b32 s10, v240, 12
	v_mov_b32_e32 v5, v3
	v_readlane_b32 s11, v240, 13
	v_lshlrev_b32_e32 v19, 4, v82
	s_add_i32 s89, s8, 0xc000
	v_lshl_add_u64 v[154:155], s[10:11], 0, v[4:5]
	v_lshlrev_b32_e32 v4, 4, v161
	v_and_b32_e32 v4, 0xf0, v4
	v_add_u32_e32 v5, 32, v19
	v_xad_u32 v21, v5, v4, 0
	v_add_u32_e32 v5, 64, v19
	v_xad_u32 v22, v5, v4, 0
	v_add_u32_e32 v5, 0x60, v19
	s_add_i32 s90, s8, 0x4000
	v_xad_u32 v20, v4, v19, 0
	v_xad_u32 v23, v5, v4, 0
	v_lshlrev_b32_e32 v4, 5, v161
	v_readlane_b32 s10, v240, 60
	s_add_i32 s9, 0, 0x10800
	s_add_i32 s91, s8, 0xe000
	s_add_i32 s94, s8, 0x6000
	s_and_b32 s8, s12, 0x7fffffc0
	v_add_u32_e32 v24, s10, v4
	v_add_u32_e32 v26, s9, v4
	v_add_u32_e32 v4, s8, v162
	v_lshlrev_b32_e32 v18, 8, v161
	v_add_u32_e32 v25, s9, v7
	v_add_u32_e32 v27, s10, v7
	v_sub_u32_e32 v2, v2, v4
	v_mov_b32_e32 v16, v3
	v_mov_b32_e32 v17, v3
	v_cmp_gt_i32_e64 s[8:9], 0, v2
	v_cmp_gt_i32_e64 s[10:11], 32, v2
	v_cmp_gt_i32_e64 s[12:13], 1, v2
	v_cmp_gt_i32_e64 s[14:15], 33, v2
	v_cmp_gt_i32_e64 s[16:17], 2, v2
	v_cmp_gt_i32_e64 s[18:19], 34, v2
	v_cmp_gt_i32_e64 s[20:21], 3, v2
	v_cmp_gt_i32_e64 s[22:23], 35, v2
	v_cmp_gt_i32_e64 s[24:25], 8, v2
	v_cmp_gt_i32_e64 s[26:27], 40, v2
	v_cmp_gt_i32_e64 s[28:29], 9, v2
	v_cmp_gt_i32_e64 s[30:31], 41, v2
	v_cmp_gt_i32_e64 s[34:35], 10, v2
	v_cmp_gt_i32_e64 s[36:37], 42, v2
	v_cmp_gt_i32_e64 s[38:39], 11, v2
	v_cmp_gt_i32_e64 s[40:41], 43, v2
	v_cmp_gt_i32_e64 s[42:43], 16, v2
	v_cmp_gt_i32_e64 s[44:45], 48, v2
	v_cmp_gt_i32_e64 s[46:47], 17, v2
	v_cmp_gt_i32_e64 s[48:49], 49, v2
	v_cmp_gt_i32_e64 s[50:51], 18, v2
	v_cmp_gt_i32_e64 s[52:53], 50, v2
	v_cmp_gt_i32_e64 s[54:55], 19, v2
	v_cmp_gt_i32_e64 s[56:57], 51, v2
	v_cmp_gt_i32_e64 s[58:59], 24, v2
	v_cmp_gt_i32_e64 s[60:61], 56, v2
	v_cmp_gt_i32_e64 s[62:63], 25, v2
	v_cmp_gt_i32_e64 s[64:65], 57, v2
	v_cmp_gt_i32_e64 s[66:67], 26, v2
	v_cmp_gt_i32_e64 s[68:69], 58, v2
	v_cmp_gt_i32_e64 s[70:71], 27, v2
	v_cmp_gt_i32_e64 s[72:73], 59, v2
	v_mov_b32_e32 v2, v3
	v_mov_b32_e32 v4, v3
	v_mov_b32_e32 v5, v3
	v_mov_b32_e32 v6, v3
	v_mov_b32_e32 v7, v3
	v_mov_b32_e32 v8, v3
	v_mov_b32_e32 v9, v3
	v_mov_b32_e32 v10, v3
	v_mov_b32_e32 v11, v3
	v_mov_b32_e32 v12, v3
	v_mov_b32_e32 v13, v3
	v_mov_b32_e32 v14, v3
	v_mov_b32_e32 v15, v3
	v_add_u32_e32 v170, v24, v19
	v_add_u32_e32 v171, v25, v84
	v_add_u32_e32 v172, v26, v19
	v_add_u32_e32 v173, v27, v84
	v_add_u32_e32 v174, v20, v18
	v_add_u32_e32 v175, v21, v18
	v_add_u32_e32 v176, v22, v18
	v_add_u32_e32 v177, v23, v18
	v_mov_b64_e32 v[32:33], v[16:17]
	v_mov_b64_e32 v[48:49], v[16:17]
	v_mov_b64_e32 v[64:65], v[16:17]
	v_mov_b64_e32 v[80:81], v[16:17]
	s_add_i32 s78, s74, 0x80
	s_add_i32 s95, s88, -1
	v_mov_b32_e32 v178, 0
	v_mov_b32_e32 v169, 0xf149f2ca
	v_mov_b64_e32 v[30:31], v[14:15]
	v_mov_b64_e32 v[28:29], v[12:13]
	v_mov_b64_e32 v[26:27], v[10:11]
	v_mov_b64_e32 v[24:25], v[8:9]
	v_mov_b64_e32 v[22:23], v[6:7]
	v_mov_b64_e32 v[20:21], v[4:5]
	v_mov_b64_e32 v[18:19], v[2:3]
	v_mov_b64_e32 v[46:47], v[14:15]
	v_mov_b64_e32 v[44:45], v[12:13]
	v_mov_b64_e32 v[42:43], v[10:11]
	v_mov_b64_e32 v[40:41], v[8:9]
	v_mov_b64_e32 v[38:39], v[6:7]
	v_mov_b64_e32 v[36:37], v[4:5]
	v_mov_b64_e32 v[34:35], v[2:3]
	v_mov_b64_e32 v[62:63], v[14:15]
	v_mov_b64_e32 v[60:61], v[12:13]
	v_mov_b64_e32 v[58:59], v[10:11]
	v_mov_b64_e32 v[56:57], v[8:9]
	v_mov_b64_e32 v[54:55], v[6:7]
	v_mov_b64_e32 v[52:53], v[4:5]
	v_mov_b64_e32 v[50:51], v[2:3]
	v_mov_b64_e32 v[78:79], v[14:15]
	v_mov_b64_e32 v[76:77], v[12:13]
	v_mov_b64_e32 v[74:75], v[10:11]
	v_mov_b64_e32 v[72:73], v[8:9]
	v_mov_b64_e32 v[70:71], v[6:7]
	v_mov_b64_e32 v[68:69], v[4:5]
	v_mov_b64_e32 v[66:67], v[2:3]

; template <int KB, bool EXT>
; __device__ __forceinline__ void qkt(f32x16& p0, f32x16& p1, const char* lds, int r32, int hi, const bf16x8* qr, bf16x8 qx) {
;     p0 = f32x16{}; p1 = f32x16{};
;     const char* kb[4];
; #pragma unroll
;     for (int dd = 0; dd < 4; ++dd) kb[dd] = lds + OFF_K + KB * SHM_K + KSWZ(r32, (dd * 16 + hi * 8) * 2);
; #pragma unroll
;     for (int d0 = 0; d0 < 8; ++d0) { const char* a = kb[d0 & 3] + (d0 >> 2) * 128;
;         bf16x8 b0 = *reinterpret_cast<const bf16x8*>(a);
;         bf16x8 b1 = *reinterpret_cast<const bf16x8*>(a + 32 * 256);
;         p0 = __builtin_amdgcn_mfma_f32_32x32x16_bf16(b0, qr[d0], p0, 0, 0, 0);
;         p1 = __builtin_amdgcn_mfma_f32_32x32x16_bf16(b1, qr[d0], p1, 0, 0, 0); }
;     if (EXT) { const char* xa = lds + OFF_X + KB * SHM_X + r32 * 32 + hi * 16;
;         bf16x8 x0 = *reinterpret_cast<const bf16x8*>(xa), x1 = *reinterpret_cast<const bf16x8*>(xa + 32 * 32);
;         p0 = __builtin_amdgcn_mfma_f32_32x32x16_bf16(x0, qx, p0, 0, 0, 0);
;         p1 = __builtin_amdgcn_mfma_f32_32x32x16_bf16(x1, qx, p1, 0, 0, 0); }
; }
.LBB0_1384:
	s_cmp_gt_i32 s76, s88
	s_cbranch_scc1 .LBB0_1392
	ds_read_b128 v[4:7], v174 offset:32768
	ds_read_b128 v[246:249], v174 offset:40960
	ds_read_b128 v[250:253], v175 offset:32768
	s_cmp_lg_u32 s88, s76
	s_waitcnt lgkmcnt(2)
	v_mfma_f32_32x32x16_bf16 v[98:113], v[4:7], v[114:117], 0
	ds_read_b128 v[4:7], v175 offset:40960
	s_waitcnt lgkmcnt(2)
	v_mfma_f32_32x32x16_bf16 v[82:97], v[246:249], v[114:117], 0
	ds_read_b128 v[246:249], v176 offset:32768
	s_waitcnt lgkmcnt(2)
	v_mfma_f32_32x32x16_bf16 v[98:113], v[250:253], v[118:121], v[98:113]
	ds_read_b128 v[250:253], v176 offset:40960
	s_waitcnt lgkmcnt(2)
	v_mfma_f32_32x32x16_bf16 v[82:97], v[4:7], v[118:121], v[82:97]
	ds_read_b128 v[4:7], v177 offset:32768
	s_waitcnt lgkmcnt(2)
	v_mfma_f32_32x32x16_bf16 v[98:113], v[246:249], v[122:125], v[98:113]
	ds_read_b128 v[246:249], v177 offset:40960
	s_waitcnt lgkmcnt(2)
	v_mfma_f32_32x32x16_bf16 v[82:97], v[250:253], v[122:125], v[82:97]
	ds_read_b128 v[250:253], v242 offset:32768
	s_waitcnt lgkmcnt(2)
	v_mfma_f32_32x32x16_bf16 v[98:113], v[4:7], v[126:129], v[98:113]
	ds_read_b128 v[4:7], v242 offset:40960
	s_waitcnt lgkmcnt(2)
	v_mfma_f32_32x32x16_bf16 v[82:97], v[246:249], v[126:129], v[82:97]
	ds_read_b128 v[246:249], v243 offset:32768
	v_xor_b32_e32 v242, 0x80, v174
	v_xor_b32_e32 v243, 0x80, v175
	v_xor_b32_e32 v244, 0x80, v176
	v_xor_b32_e32 v245, 0x80, v177
	s_waitcnt lgkmcnt(2)
	v_mfma_f32_32x32x16_bf16 v[98:113], v[250:253], v[130:133], v[98:113]
	ds_read_b128 v[250:253], v243 offset:40960
	s_waitcnt lgkmcnt(2)
	v_mfma_f32_32x32x16_bf16 v[82:97], v[4:7], v[130:133], v[82:97]
	ds_read_b128 v[4:7], v244 offset:32768
	s_waitcnt lgkmcnt(2)
	v_mfma_f32_32x32x16_bf16 v[98:113], v[246:249], v[134:137], v[98:113]
	ds_read_b128 v[246:249], v244 offset:40960
	s_waitcnt lgkmcnt(2)
	v_mfma_f32_32x32x16_bf16 v[82:97], v[250:253], v[134:137], v[82:97]
	ds_read_b128 v[250:253], v245 offset:32768
	s_waitcnt lgkmcnt(2)
	v_mfma_f32_32x32x16_bf16 v[98:113], v[4:7], v[138:141], v[98:113]
	ds_read_b128 v[4:7], v245 offset:40960
	s_waitcnt lgkmcnt(2)
	v_mfma_f32_32x32x16_bf16 v[82:97], v[246:249], v[138:141], v[82:97]
	ds_read_b128 v[246:249], v170
	s_waitcnt lgkmcnt(2)
	v_mfma_f32_32x32x16_bf16 v[98:113], v[250:253], v[142:145], v[98:113]
	ds_read_b128 v[250:253], v170 offset:1024
	s_waitcnt lgkmcnt(2)
	v_mfma_f32_32x32x16_bf16 v[82:97], v[4:7], v[142:145], v[82:97]
	s_waitcnt vmcnt(0)
	s_waitcnt lgkmcnt(1)
	v_mfma_f32_32x32x16_bf16 v[98:113], v[246:249], v[146:149], v[98:113]
	s_waitcnt lgkmcnt(0)
	v_mfma_f32_32x32x16_bf16 v[82:97], v[250:253], v[146:149], v[82:97]
	s_cbranch_scc1 .LBB0_1387
	s_and_b64 vcc, s[70:71], s[66:67]
	s_nop 6
	v_cndmask_b32_e32 v112, v112, v159, vcc
	s_and_b64 vcc, vcc, s[62:63]
	v_cndmask_b32_e32 v111, v111, v159, vcc
	s_and_b64 vcc, vcc, s[58:59]
	v_cndmask_b32_e32 v110, v110, v159, vcc
	s_and_b64 vcc, vcc, s[54:55]
	v_cndmask_b32_e32 v109, v109, v159, vcc
	s_and_b64 vcc, vcc, s[50:51]
	v_cndmask_b32_e32 v108, v108, v159, vcc
	s_and_b64 vcc, vcc, s[46:47]
	v_cndmask_b32_e32 v107, v107, v159, vcc
	s_and_b64 vcc, vcc, s[42:43]
	v_cndmask_b32_e32 v106, v106, v159, vcc
	s_and_b64 vcc, vcc, s[38:39]
	v_cndmask_b32_e32 v105, v105, v159, vcc
	s_and_b64 vcc, vcc, s[34:35]
	v_cndmask_b32_e32 v104, v104, v159, vcc
	s_and_b64 vcc, vcc, s[28:29]
	v_cndmask_b32_e32 v103, v103, v159, vcc
	s_and_b64 vcc, vcc, s[24:25]
	v_cndmask_b32_e32 v102, v102, v159, vcc
	s_and_b64 vcc, vcc, s[20:21]
	v_cndmask_b32_e32 v101, v101, v159, vcc
	s_and_b64 vcc, vcc, s[16:17]
	v_cndmask_b32_e32 v100, v100, v159, vcc
	s_and_b64 vcc, vcc, s[12:13]
	v_cndmask_b32_e32 v99, v99, v159, vcc
	s_and_b64 vcc, vcc, s[8:9]
	v_cndmask_b32_e32 v98, v98, v159, vcc
	s_and_b64 vcc, s[72:73], s[68:69]
	v_cndmask_b32_e32 v96, v96, v159, vcc
	s_and_b64 vcc, vcc, s[64:65]
	v_cndmask_b32_e32 v95, v95, v159, vcc
	s_and_b64 vcc, vcc, s[60:61]
	v_cndmask_b32_e32 v94, v94, v159, vcc
	s_and_b64 vcc, vcc, s[56:57]
	v_cndmask_b32_e32 v93, v93, v159, vcc
	s_and_b64 vcc, vcc, s[52:53]
	v_cndmask_b32_e32 v92, v92, v159, vcc
	s_and_b64 vcc, vcc, s[48:49]
	v_cndmask_b32_e32 v91, v91, v159, vcc
	s_and_b64 vcc, vcc, s[44:45]
	v_cndmask_b32_e32 v90, v90, v159, vcc
	s_and_b64 vcc, vcc, s[40:41]
	v_cndmask_b32_e32 v89, v89, v159, vcc
	s_and_b64 vcc, vcc, s[36:37]
	v_cndmask_b32_e32 v88, v88, v159, vcc
	s_and_b64 vcc, vcc, s[30:31]
	v_cndmask_b32_e32 v87, v87, v159, vcc
	s_and_b64 vcc, vcc, s[26:27]
	v_cndmask_b32_e32 v86, v86, v159, vcc
	s_and_b64 vcc, vcc, s[22:23]
	v_cndmask_b32_e32 v85, v85, v159, vcc
	s_and_b64 vcc, vcc, s[18:19]
	v_cndmask_b32_e32 v84, v84, v159, vcc
	s_and_b64 vcc, vcc, s[14:15]
	v_cndmask_b32_e32 v83, v83, v159, vcc
	s_and_b64 vcc, vcc, s[10:11]
	v_cndmask_b32_e64 v113, v113, v159, s[70:71]
	v_cndmask_b32_e64 v97, v97, v159, s[72:73]
	v_cndmask_b32_e32 v82, v82, v159, vcc

; template <int KB, bool EXT>
; __device__ __forceinline__ void qkt(f32x16& p0, f32x16& p1, const char* lds, int r32, int hi, const bf16x8* qr, bf16x8 qx) {
;     p0 = f32x16{}; p1 = f32x16{};
;     const char* kb[4];
; #pragma unroll
;     for (int dd = 0; dd < 4; ++dd) kb[dd] = lds + OFF_K + KB * SHM_K + KSWZ(r32, (dd * 16 + hi * 8) * 2);
; #pragma unroll
;     for (int d0 = 0; d0 < 8; ++d0) { const char* a = kb[d0 & 3] + (d0 >> 2) * 128;
;         bf16x8 b0 = *reinterpret_cast<const bf16x8*>(a);
;         bf16x8 b1 = *reinterpret_cast<const bf16x8*>(a + 32 * 256);
;         p0 = __builtin_amdgcn_mfma_f32_32x32x16_bf16(b0, qr[d0], p0, 0, 0, 0);
;         p1 = __builtin_amdgcn_mfma_f32_32x32x16_bf16(b1, qr[d0], p1, 0, 0, 0); }
;     if (EXT) { const char* xa = lds + OFF_X + KB * SHM_X + r32 * 32 + hi * 16;
;         bf16x8 x0 = *reinterpret_cast<const bf16x8*>(xa), x1 = *reinterpret_cast<const bf16x8*>(xa + 32 * 32);
;         p0 = __builtin_amdgcn_mfma_f32_32x32x16_bf16(x0, qx, p0, 0, 0, 0);
;         p1 = __builtin_amdgcn_mfma_f32_32x32x16_bf16(x1, qx, p1, 0, 0, 0); }
; }
.LBB0_1398:
	s_cmp_ge_i32 s76, s88
	s_cbranch_scc1 .LBB0_1406
	ds_read_b128 v[4:7], v174 offset:49152
	ds_read_b128 v[246:249], v174 offset:57344
	ds_read_b128 v[250:253], v175 offset:49152
	s_cmp_lg_u32 s95, s76
	s_waitcnt lgkmcnt(2)
	v_mfma_f32_32x32x16_bf16 v[98:113], v[4:7], v[114:117], 0
	ds_read_b128 v[4:7], v175 offset:57344
	s_waitcnt lgkmcnt(2)
	v_mfma_f32_32x32x16_bf16 v[82:97], v[246:249], v[114:117], 0
	ds_read_b128 v[246:249], v176 offset:49152
	s_waitcnt lgkmcnt(2)
	v_mfma_f32_32x32x16_bf16 v[98:113], v[250:253], v[118:121], v[98:113]
	ds_read_b128 v[250:253], v176 offset:57344
	s_waitcnt lgkmcnt(2)
	v_mfma_f32_32x32x16_bf16 v[82:97], v[4:7], v[118:121], v[82:97]
	ds_read_b128 v[4:7], v177 offset:49152
	s_waitcnt lgkmcnt(2)
	v_mfma_f32_32x32x16_bf16 v[98:113], v[246:249], v[122:125], v[98:113]
	ds_read_b128 v[246:249], v177 offset:57344
	s_waitcnt lgkmcnt(2)
	v_mfma_f32_32x32x16_bf16 v[82:97], v[250:253], v[122:125], v[82:97]
	ds_read_b128 v[250:253], v242 offset:49152
	s_waitcnt lgkmcnt(2)
	v_mfma_f32_32x32x16_bf16 v[98:113], v[4:7], v[126:129], v[98:113]
	ds_read_b128 v[4:7], v242 offset:57344
	s_waitcnt lgkmcnt(2)
	v_mfma_f32_32x32x16_bf16 v[82:97], v[246:249], v[126:129], v[82:97]
	ds_read_b128 v[246:249], v243 offset:49152
	v_xor_b32_e32 v242, 0x80, v174
	v_xor_b32_e32 v243, 0x80, v175
	v_xor_b32_e32 v244, 0x80, v176
	v_xor_b32_e32 v245, 0x80, v177
	s_waitcnt lgkmcnt(2)
	v_mfma_f32_32x32x16_bf16 v[98:113], v[250:253], v[130:133], v[98:113]
	ds_read_b128 v[250:253], v243 offset:57344
	s_waitcnt lgkmcnt(2)
	v_mfma_f32_32x32x16_bf16 v[82:97], v[4:7], v[130:133], v[82:97]
	ds_read_b128 v[4:7], v244 offset:49152
	s_waitcnt lgkmcnt(2)
	v_mfma_f32_32x32x16_bf16 v[98:113], v[246:249], v[134:137], v[98:113]
	ds_read_b128 v[246:249], v244 offset:57344
	s_waitcnt lgkmcnt(2)
	v_mfma_f32_32x32x16_bf16 v[82:97], v[250:253], v[134:137], v[82:97]
	ds_read_b128 v[250:253], v245 offset:49152
	s_waitcnt lgkmcnt(2)
	v_mfma_f32_32x32x16_bf16 v[98:113], v[4:7], v[138:141], v[98:113]
	ds_read_b128 v[4:7], v245 offset:57344
	s_waitcnt lgkmcnt(2)
	v_mfma_f32_32x32x16_bf16 v[82:97], v[246:249], v[138:141], v[82:97]
	ds_read_b128 v[246:249], v172
	s_waitcnt lgkmcnt(2)
	v_mfma_f32_32x32x16_bf16 v[98:113], v[250:253], v[142:145], v[98:113]
	ds_read_b128 v[250:253], v172 offset:1024
	s_waitcnt lgkmcnt(2)
	v_mfma_f32_32x32x16_bf16 v[82:97], v[4:7], v[142:145], v[82:97]
	s_waitcnt vmcnt(0)
	s_waitcnt lgkmcnt(1)
	v_mfma_f32_32x32x16_bf16 v[98:113], v[246:249], v[146:149], v[98:113]
	s_waitcnt lgkmcnt(0)
	v_mfma_f32_32x32x16_bf16 v[82:97], v[250:253], v[146:149], v[82:97]
	s_cbranch_scc1 .LBB0_1401
	s_and_b64 vcc, s[70:71], s[66:67]
	s_nop 6
	v_cndmask_b32_e32 v112, v112, v159, vcc
	s_and_b64 vcc, vcc, s[62:63]
	v_cndmask_b32_e32 v111, v111, v159, vcc
	s_and_b64 vcc, vcc, s[58:59]
	v_cndmask_b32_e32 v110, v110, v159, vcc
	s_and_b64 vcc, vcc, s[54:55]
	v_cndmask_b32_e32 v109, v109, v159, vcc
	s_and_b64 vcc, vcc, s[50:51]
	v_cndmask_b32_e32 v108, v108, v159, vcc
	s_and_b64 vcc, vcc, s[46:47]
	v_cndmask_b32_e32 v107, v107, v159, vcc
	s_and_b64 vcc, vcc, s[42:43]
	v_cndmask_b32_e32 v106, v106, v159, vcc
	s_and_b64 vcc, vcc, s[38:39]
	v_cndmask_b32_e32 v105, v105, v159, vcc
	s_and_b64 vcc, vcc, s[34:35]
	v_cndmask_b32_e32 v104, v104, v159, vcc
	s_and_b64 vcc, vcc, s[28:29]
	v_cndmask_b32_e32 v103, v103, v159, vcc
	s_and_b64 vcc, vcc, s[24:25]
	v_cndmask_b32_e32 v102, v102, v159, vcc
	s_and_b64 vcc, vcc, s[20:21]
	v_cndmask_b32_e32 v101, v101, v159, vcc
	s_and_b64 vcc, vcc, s[16:17]
	v_cndmask_b32_e32 v100, v100, v159, vcc
	s_and_b64 vcc, vcc, s[12:13]
	v_cndmask_b32_e32 v99, v99, v159, vcc
	s_and_b64 vcc, vcc, s[8:9]
	v_cndmask_b32_e32 v98, v98, v159, vcc
	s_and_b64 vcc, s[72:73], s[68:69]
	v_cndmask_b32_e32 v96, v96, v159, vcc
	s_and_b64 vcc, vcc, s[64:65]
	v_cndmask_b32_e32 v95, v95, v159, vcc
	s_and_b64 vcc, vcc, s[60:61]
	v_cndmask_b32_e32 v94, v94, v159, vcc
	s_and_b64 vcc, vcc, s[56:57]
	v_cndmask_b32_e32 v93, v93, v159, vcc
	s_and_b64 vcc, vcc, s[52:53]
	v_cndmask_b32_e32 v92, v92, v159, vcc
	s_and_b64 vcc, vcc, s[48:49]
	v_cndmask_b32_e32 v91, v91, v159, vcc
	s_and_b64 vcc, vcc, s[44:45]
	v_cndmask_b32_e32 v90, v90, v159, vcc
	s_and_b64 vcc, vcc, s[40:41]
	v_cndmask_b32_e32 v89, v89, v159, vcc
	s_and_b64 vcc, vcc, s[36:37]
	v_cndmask_b32_e32 v88, v88, v159, vcc
	s_and_b64 vcc, vcc, s[30:31]
	v_cndmask_b32_e32 v87, v87, v159, vcc
	s_and_b64 vcc, vcc, s[26:27]
	v_cndmask_b32_e32 v86, v86, v159, vcc
	s_and_b64 vcc, vcc, s[22:23]
	v_cndmask_b32_e32 v85, v85, v159, vcc
	s_and_b64 vcc, vcc, s[18:19]
	v_cndmask_b32_e32 v84, v84, v159, vcc
	s_and_b64 vcc, vcc, s[14:15]
	v_cndmask_b32_e32 v83, v83, v159, vcc
	s_and_b64 vcc, vcc, s[10:11]
	v_cndmask_b32_e64 v113, v113, v159, s[70:71]
	v_cndmask_b32_e64 v97, v97, v159, s[72:73]
	v_cndmask_b32_e32 v82, v82, v159, vcc

; __global__ void __launch_bounds__(NTHREADS, 2) mega_fwd(Args args) {
	.amdhsa_kernel _Z8mega_fwd4Args
		.amdhsa_group_segment_fixed_size 0
		.amdhsa_private_segment_fixed_size 0
		.amdhsa_kernarg_size 448
		.amdhsa_user_sgpr_count 2
		.amdhsa_user_sgpr_dispatch_ptr 0
		.amdhsa_user_sgpr_queue_ptr 0
		.amdhsa_user_sgpr_kernarg_segment_ptr 1
		.amdhsa_user_sgpr_dispatch_id 0
		.amdhsa_user_sgpr_kernarg_preload_length 0
		.amdhsa_user_sgpr_kernarg_preload_offset 0
		.amdhsa_user_sgpr_private_segment_size 0
		.amdhsa_uses_dynamic_stack 0
		.amdhsa_enable_private_segment 0
		.amdhsa_system_sgpr_workgroup_id_x 1
		.amdhsa_system_sgpr_workgroup_id_y 0
		.amdhsa_system_sgpr_workgroup_id_z 0
		.amdhsa_system_sgpr_workgroup_info 0
		.amdhsa_system_vgpr_workitem_id 0
		.amdhsa_next_free_vgpr 254
		.amdhsa_next_free_sgpr 100
		.amdhsa_accum_offset 256
		.amdhsa_reserve_vcc 1
		.amdhsa_float_round_mode_32 0
		.amdhsa_float_round_mode_16_64 0
		.amdhsa_float_denorm_mode_32 3
		.amdhsa_float_denorm_mode_16_64 3
		.amdhsa_dx10_clamp 1
		.amdhsa_ieee_mode 1
		.amdhsa_fp16_overflow 0
		.amdhsa_tg_split 0
		.amdhsa_exception_fp_ieee_invalid_op 0
		.amdhsa_exception_fp_denorm_src 0
		.amdhsa_exception_fp_ieee_div_zero 0
		.amdhsa_exception_fp_ieee_overflow 0
		.amdhsa_exception_fp_ieee_underflow 0
		.amdhsa_exception_fp_ieee_inexact 0
		.amdhsa_exception_int_div_zero 0
	.end_amdhsa_kernel

; __global__ void __launch_bounds__(NTHREADS, 2) mega_fwd(Args args) {
amdhsa.kernels:
  - .agpr_count:     0
    .args:
      - .offset:         0
        .size:           192
        .value_kind:     by_value
      - .offset:         192
        .size:           4
        .value_kind:     hidden_block_count_x
      - .offset:         196
        .size:           4
        .value_kind:     hidden_block_count_y
      - .offset:         200
        .size:           4
        .value_kind:     hidden_block_count_z
      - .offset:         204
        .size:           2
        .value_kind:     hidden_group_size_x
      - .offset:         206
        .size:           2
        .value_kind:     hidden_group_size_y
      - .offset:         208
        .size:           2
        .value_kind:     hidden_group_size_z
      - .offset:         210
        .size:           2
        .value_kind:     hidden_remainder_x
      - .offset:         212
        .size:           2
        .value_kind:     hidden_remainder_y
      - .offset:         214
        .size:           2
        .value_kind:     hidden_remainder_z
      - .offset:         232
        .size:           8
        .value_kind:     hidden_global_offset_x
      - .offset:         240
        .size:           8
        .value_kind:     hidden_global_offset_y
      - .offset:         248
        .size:           8
        .value_kind:     hidden_global_offset_z
      - .offset:         256
        .size:           2
        .value_kind:     hidden_grid_dims
      - .offset:         312
        .size:           4
        .value_kind:     hidden_dynamic_lds_size
    .group_segment_fixed_size: 0
    .kernarg_segment_align: 8
    .kernarg_segment_size: 448
    .language:       OpenCL C
    .language_version:
      - 2
      - 0
    .max_flat_workgroup_size: 512
    .name:           _Z8mega_fwd4Args
    .private_segment_fixed_size: 0
    .sgpr_count:     106
    .sgpr_spill_count: 332
    .symbol:         _Z8mega_fwd4Args.kd
    .uniform_work_group_size: 1
    .uses_dynamic_stack: false
    .vgpr_count:     254
    .vgpr_spill_count: 0
    .wavefront_size: 64
